# v40_gfirst
# speedup vs baseline: 1.0046x; 1.0046x over previous
.LBB3_4:
	s_ashr_i32 s20, s3, 31
	s_mov_b32 s50, 0
	s_lshr_b32 s20, s20, 26
	s_add_i32 s20, s3, s20
	s_ashr_i32 s51, s50, 31
	s_ashr_i32 s94, s20, 6
	s_lshl_b64 s[56:57], s[50:51], 1
	s_add_u32 s20, s36, s56
	s_addc_u32 s21, s37, s57
	s_add_u32 s56, s30, s56
	s_addc_u32 s57, s31, s57
	v_lshl_add_u64 v[18:19], s[56:57], 0, v[108:109]
	v_add_co_u32_e32 v2, vcc, s35, v18
	s_nop 1
	v_addc_co_u32_e32 v3, vcc, 0, v19, vcc
	v_add_co_u32_e32 v4, vcc, s41, v18
	s_barrier
	s_nop 0
	v_addc_co_u32_e32 v5, vcc, 0, v19, vcc
	s_mul_i32 s95, s94, 0x50
	v_add_u32_e32 v42, s95, v1
	s_mul_i32 s58, s94, 0xffe9a800
	v_max_i32_e32 v42, 3, v42
	s_add_i32 s58, s58, s29
	v_add_u32_e32 v42, -3, v42
	v_add_u32_e32 v44, s95, v112
	v_min_u32_e32 v66, 0x400, v42
	v_add_u32_e32 v42, s58, v133
	v_max_i32_e32 v44, 3, v44
	v_ashrrev_i32_e32 v43, 31, v42
	v_add_u32_e32 v44, -3, v44
	v_lshl_add_u64 v[42:43], v[66:67], 0, v[42:43]
	v_min_u32_e32 v66, 0x400, v44
	v_add_u32_e32 v44, s58, v132
	v_ashrrev_i32_e32 v45, 31, v44
	v_lshl_add_u64 v[42:43], v[42:43], 4, s[20:21]
	v_lshl_add_u64 v[44:45], v[66:67], 0, v[44:45]
	v_lshl_add_u64 v[44:45], v[44:45], 4, s[20:21]
	global_load_dwordx4 v[62:65], v[42:43], off
	global_load_dwordx4 v[58:61], v[44:45], off
	v_add_u32_e32 v42, s95, v113
	v_max_i32_e32 v42, 3, v42
	v_add_u32_e32 v42, -3, v42
	v_add_u32_e32 v44, s95, v114
	v_min_u32_e32 v66, 0x400, v42
	v_add_u32_e32 v42, s58, v131
	v_max_i32_e32 v44, 3, v44
	v_ashrrev_i32_e32 v43, 31, v42
	v_add_u32_e32 v44, -3, v44
	v_lshl_add_u64 v[42:43], v[66:67], 0, v[42:43]
	v_min_u32_e32 v66, 0x400, v44
	v_add_u32_e32 v44, s58, v130
	v_ashrrev_i32_e32 v45, 31, v44
	v_lshl_add_u64 v[42:43], v[42:43], 4, s[20:21]
	v_lshl_add_u64 v[44:45], v[66:67], 0, v[44:45]
	v_lshl_add_u64 v[44:45], v[44:45], 4, s[20:21]
	global_load_dwordx4 v[54:57], v[42:43], off
	global_load_dwordx4 v[50:53], v[44:45], off
	v_add_u32_e32 v42, s95, v115
	v_max_i32_e32 v42, 3, v42
	v_add_u32_e32 v42, -3, v42
	v_add_u32_e32 v44, s95, v116
	v_min_u32_e32 v66, 0x400, v42
	v_add_u32_e32 v42, s58, v105
	v_max_i32_e32 v44, 3, v44
	v_ashrrev_i32_e32 v43, 31, v42
	v_add_u32_e32 v44, -3, v44
	v_lshl_add_u64 v[42:43], v[66:67], 0, v[42:43]
	v_min_u32_e32 v66, 0x400, v44
	v_add_u32_e32 v44, s58, v99
	v_ashrrev_i32_e32 v45, 31, v44
	v_lshl_add_u64 v[44:45], v[66:67], 0, v[44:45]
	v_lshl_add_u64 v[42:43], v[42:43], 4, s[20:21]
	v_lshl_add_u64 v[44:45], v[44:45], 4, s[20:21]
	global_load_dwordx4 v[46:49], v[42:43], off
	global_load_dwordx4 v[42:45], v[44:45], off
	global_load_dwordx4 v[22:25], v106, s[56:57]
	global_load_dwordx4 v[26:29], v[2:3], off offset:1024
	global_load_dwordx4 v[30:33], v[4:5], off offset:2048
	v_add_co_u32_e32 v2, vcc, s43, v18
	s_nop 0
	v_addc_co_u32_e32 v3, vcc, 0, v19, vcc
	v_add_co_u32_e32 v4, vcc, s45, v18
	s_nop 0
	v_addc_co_u32_e32 v5, vcc, 0, v19, vcc
	global_load_dwordx4 v[34:37], v[2:3], off offset:3072
	global_load_dwordx4 v[38:41], v[4:5], off
	v_add_co_u32_e32 v2, vcc, s47, v18
	s_nop 0
	v_addc_co_u32_e32 v3, vcc, 0, v19, vcc
	v_add_co_u32_e32 v6, vcc, s33, v18
	s_nop 0
	v_addc_co_u32_e32 v7, vcc, 0, v19, vcc
	v_add_co_u32_e32 v10, vcc, s49, v18
	v_addc_co_u32_e32 v11, vcc, 0, v19, vcc
	v_add_co_u32_e32 v14, vcc, s60, v18
	v_addc_co_u32_e32 v15, vcc, 0, v19, vcc
	v_add_co_u32_e32 v18, vcc, s61, v18
	s_nop 0
	v_addc_co_u32_e32 v19, vcc, 0, v19, vcc
	global_load_dwordx4 v[2:5], v[2:3], off offset:1024
	s_nop 0
	global_load_dwordx4 v[6:9], v[6:7], off offset:2048
	s_nop 0
	global_load_dwordx4 v[10:13], v[10:11], off offset:3072
	s_nop 0
	global_load_dwordx4 v[14:17], v[14:15], off
	global_load_dwordx4 v[18:21], v[18:19], off offset:1024
	s_nop 0
	s_nop 0
	s_cmp_gt_i32 s3, 63
	s_cbranch_scc0 .LBB3_22
	s_and_saveexec_b64 s[58:59], s[8:9]

.LBB3_8:
	s_or_b64 exec, exec, s[20:21]
	s_waitcnt lgkmcnt(0)
	s_barrier
	ds_read_b128 v[152:155], v69 offset:62400
	ds_read_b128 v[156:159], v69 offset:63104
	s_waitcnt vmcnt(15)
	v_cvt_f32_f16_sdwa v111, v62 dst_sel:DWORD dst_unused:UNUSED_PAD src0_sel:WORD_1
	v_cvt_f32_f16_e32 v110, v62
	s_add_i32 s58, s95, -3
	v_add_u32_e32 v66, s58, v1
	v_cmp_gt_u32_e32 vcc, s73, v66
	s_waitcnt lgkmcnt(0)
	v_pk_fma_f32 v[110:111], v[110:111], v[152:153], v[156:157]
	ds_read_b128 v[160:163], v69 offset:62416
	ds_read_b128 v[164:167], v69 offset:63120
	v_pk_mul_f32 v[152:153], v[110:111], s[28:29] op_sel_hi:[1,0]
	v_pk_mul_f32 v[170:171], v[110:111], 0.5 op_sel_hi:[1,0]
	v_fma_f32 v62, |v152|, s74, 1.0
	v_fma_f32 v107, |v153|, s74, 1.0
	v_rcp_f32_e32 v156, v62
	v_rcp_f32_e32 v157, v107
	v_mul_f32_e64 v62, |v152|, -|v152|
	v_mul_f32_e32 v62, 0x3fb8aa3b, v62
	v_exp_f32_e32 v168, v62
	v_mov_b64_e32 v[110:111], s[34:35]
	v_mul_f32_e64 v62, |v153|, -|v153|
	v_pk_fma_f32 v[172:173], v[156:157], s[40:41], v[110:111] op_sel_hi:[1,0,0]
	v_mul_f32_e32 v62, 0x3fb8aa3b, v62
	v_pk_fma_f32 v[172:173], v[156:157], v[172:173], s[42:43] op_sel_hi:[1,1,0]
	v_exp_f32_e32 v169, v62
	v_pk_fma_f32 v[172:173], v[156:157], v[172:173], s[44:45] op_sel_hi:[1,1,0]
	v_cndmask_b32_e64 v66, 0, 1.0, vcc
	v_pk_fma_f32 v[172:173], v[156:157], v[172:173], s[46:47] op_sel_hi:[1,1,0]
	s_nop 0
	v_pk_mul_f32 v[156:157], v[172:173], v[156:157] neg_lo:[0,1] neg_hi:[0,1]
	s_nop 0
	v_pk_fma_f32 v[156:157], v[156:157], v[168:169], 1.0 op_sel_hi:[1,1,0]
	s_nop 0
	v_bfi_b32 v153, s71, v157, v153
	v_bfi_b32 v152, s71, v156, v152
	v_cvt_f32_f16_sdwa v157, v63 dst_sel:DWORD dst_unused:UNUSED_PAD src0_sel:WORD_1
	v_cvt_f32_f16_e32 v156, v63
	v_pk_add_f32 v[152:153], v[152:153], 1.0 op_sel_hi:[1,0]
	s_nop 0
	v_pk_mul_f32 v[62:63], v[170:171], v[152:153]
	v_pk_fma_f32 v[152:153], v[156:157], v[154:155], v[158:159]
	v_pk_mul_f32 v[62:63], v[66:67], v[62:63] op_sel_hi:[0,1]
	v_pk_mul_f32 v[154:155], v[152:153], s[28:29] op_sel_hi:[1,0]
	v_cvt_pk_f16_f32 v62, v62, v63
	v_fma_f32 v63, |v154|, s74, 1.0
	v_fma_f32 v107, |v155|, s74, 1.0
	v_rcp_f32_e32 v156, v63
	v_rcp_f32_e32 v157, v107
	v_mul_f32_e64 v63, |v154|, -|v154|
	v_mul_f32_e32 v63, 0x3fb8aa3b, v63
	v_exp_f32_e32 v158, v63
	v_mul_f32_e64 v63, |v155|, -|v155|
	v_pk_fma_f32 v[168:169], v[156:157], s[40:41], v[110:111] op_sel_hi:[1,0,0]
	v_mul_f32_e32 v63, 0x3fb8aa3b, v63
	v_pk_fma_f32 v[168:169], v[156:157], v[168:169], s[42:43] op_sel_hi:[1,1,0]
	v_exp_f32_e32 v159, v63
	v_pk_fma_f32 v[168:169], v[156:157], v[168:169], s[44:45] op_sel_hi:[1,1,0]
	v_pk_mul_f32 v[152:153], v[152:153], 0.5 op_sel_hi:[1,0]
	v_pk_fma_f32 v[168:169], v[156:157], v[168:169], s[46:47] op_sel_hi:[1,1,0]
	s_nop 0
	v_pk_mul_f32 v[156:157], v[168:169], v[156:157] neg_lo:[0,1] neg_hi:[0,1]
	s_nop 0
	v_pk_fma_f32 v[156:157], v[156:157], v[158:159], 1.0 op_sel_hi:[1,1,0]
	s_nop 0
	v_bfi_b32 v155, s71, v157, v155
	v_bfi_b32 v154, s71, v156, v154
	v_cvt_f32_f16_sdwa v157, v64 dst_sel:DWORD dst_unused:UNUSED_PAD src0_sel:WORD_1
	v_cvt_f32_f16_e32 v156, v64
	v_pk_add_f32 v[154:155], v[154:155], 1.0 op_sel_hi:[1,0]
	s_nop 0
	v_pk_mul_f32 v[152:153], v[152:153], v[154:155]
	s_nop 0
	v_pk_mul_f32 v[152:153], v[66:67], v[152:153] op_sel_hi:[0,1]
	v_cvt_pk_f16_f32 v63, v152, v153
	s_waitcnt lgkmcnt(0)
	v_pk_fma_f32 v[152:153], v[156:157], v[160:161], v[164:165]
	s_waitcnt vmcnt(14)
	v_cvt_f32_f16_sdwa v165, v58 dst_sel:DWORD dst_unused:UNUSED_PAD src0_sel:WORD_1
	v_pk_mul_f32 v[154:155], v[152:153], s[28:29] op_sel_hi:[1,0]
	v_pk_mul_f32 v[152:153], v[152:153], 0.5 op_sel_hi:[1,0]
	v_fma_f32 v64, |v154|, s74, 1.0
	v_fma_f32 v107, |v155|, s74, 1.0
	v_rcp_f32_e32 v156, v64
	v_rcp_f32_e32 v157, v107
	v_mul_f32_e64 v64, |v154|, -|v154|
	v_mul_f32_e32 v64, 0x3fb8aa3b, v64
	v_exp_f32_e32 v158, v64
	v_mul_f32_e64 v64, |v155|, -|v155|
	v_pk_fma_f32 v[160:161], v[156:157], s[40:41], v[110:111] op_sel_hi:[1,0,0]
	v_mul_f32_e32 v64, 0x3fb8aa3b, v64
	v_pk_fma_f32 v[160:161], v[156:157], v[160:161], s[42:43] op_sel_hi:[1,1,0]
	v_exp_f32_e32 v159, v64
	v_pk_fma_f32 v[160:161], v[156:157], v[160:161], s[44:45] op_sel_hi:[1,1,0]
	v_cvt_f32_f16_e32 v164, v58
	v_pk_fma_f32 v[160:161], v[156:157], v[160:161], s[46:47] op_sel_hi:[1,1,0]
	s_nop 0
	v_pk_mul_f32 v[156:157], v[160:161], v[156:157] neg_lo:[0,1] neg_hi:[0,1]
	s_nop 0
	v_pk_fma_f32 v[156:157], v[156:157], v[158:159], 1.0 op_sel_hi:[1,1,0]
	s_nop 0
	v_bfi_b32 v155, s71, v157, v155
	v_bfi_b32 v154, s71, v156, v154
	v_cvt_f32_f16_sdwa v157, v65 dst_sel:DWORD dst_unused:UNUSED_PAD src0_sel:WORD_1
	v_cvt_f32_f16_e32 v156, v65
	v_pk_add_f32 v[154:155], v[154:155], 1.0 op_sel_hi:[1,0]
	s_nop 0
	v_pk_mul_f32 v[64:65], v[152:153], v[154:155]
	v_pk_fma_f32 v[152:153], v[156:157], v[162:163], v[166:167]
	v_pk_mul_f32 v[64:65], v[66:67], v[64:65] op_sel_hi:[0,1]
	v_pk_mul_f32 v[154:155], v[152:153], s[28:29] op_sel_hi:[1,0]
	v_cvt_pk_f16_f32 v64, v64, v65
	v_fma_f32 v65, |v154|, s74, 1.0
	v_fma_f32 v107, |v155|, s74, 1.0
	v_rcp_f32_e32 v156, v65
	v_rcp_f32_e32 v157, v107
	v_mul_f32_e64 v65, |v154|, -|v154|
	v_mul_f32_e32 v65, 0x3fb8aa3b, v65
	v_exp_f32_e32 v158, v65
	v_mul_f32_e64 v65, |v155|, -|v155|
	v_pk_fma_f32 v[160:161], v[156:157], s[40:41], v[110:111] op_sel_hi:[1,0,0]
	v_mul_f32_e32 v65, 0x3fb8aa3b, v65
	v_pk_fma_f32 v[160:161], v[156:157], v[160:161], s[42:43] op_sel_hi:[1,1,0]
	v_exp_f32_e32 v159, v65
	v_pk_fma_f32 v[160:161], v[156:157], v[160:161], s[44:45] op_sel_hi:[1,1,0]
	v_pk_mul_f32 v[152:153], v[152:153], 0.5 op_sel_hi:[1,0]
	v_pk_fma_f32 v[160:161], v[156:157], v[160:161], s[46:47] op_sel_hi:[1,1,0]
	s_nop 0
	v_pk_mul_f32 v[156:157], v[160:161], v[156:157] neg_lo:[0,1] neg_hi:[0,1]
	s_nop 0
	v_pk_fma_f32 v[156:157], v[156:157], v[158:159], 1.0 op_sel_hi:[1,1,0]
	s_nop 0
	v_bfi_b32 v155, s71, v157, v155
	v_bfi_b32 v154, s71, v156, v154
	v_pk_add_f32 v[154:155], v[154:155], 1.0 op_sel_hi:[1,0]
	s_nop 0
	v_pk_mul_f32 v[152:153], v[152:153], v[154:155]
	s_nop 0
	v_pk_mul_f32 v[152:153], v[66:67], v[152:153] op_sel_hi:[0,1]
	v_cvt_pk_f16_f32 v65, v152, v153
	ds_write_b128 v138, v[62:65]
	ds_read_b128 v[62:65], v118 offset:62400
	ds_read_b128 v[152:155], v118 offset:63104
	v_add_u32_e32 v66, s58, v112
	v_cmp_gt_u32_e32 vcc, s73, v66
	ds_read_b128 v[156:159], v118 offset:62416
	ds_read_b128 v[160:163], v118 offset:63120
	v_cndmask_b32_e64 v66, 0, 1.0, vcc
	s_waitcnt lgkmcnt(2)
	v_pk_fma_f32 v[62:63], v[164:165], v[62:63], v[152:153]
	s_nop 0
	v_pk_mul_f32 v[152:153], v[62:63], s[28:29] op_sel_hi:[1,0]
	v_pk_mul_f32 v[62:63], v[62:63], 0.5 op_sel_hi:[1,0]
	v_fma_f32 v58, |v152|, s74, 1.0
	v_fma_f32 v107, |v153|, s74, 1.0
	v_rcp_f32_e32 v164, v58
	v_rcp_f32_e32 v165, v107
	v_mul_f32_e64 v58, |v152|, -|v152|
	v_mul_f32_e32 v58, 0x3fb8aa3b, v58
	v_exp_f32_e32 v166, v58
	v_mul_f32_e64 v58, |v153|, -|v153|
	v_pk_fma_f32 v[168:169], v[164:165], s[40:41], v[110:111] op_sel_hi:[1,0,0]
	v_mul_f32_e32 v58, 0x3fb8aa3b, v58
	v_pk_fma_f32 v[168:169], v[164:165], v[168:169], s[42:43] op_sel_hi:[1,1,0]
	v_exp_f32_e32 v167, v58
	v_pk_fma_f32 v[168:169], v[164:165], v[168:169], s[44:45] op_sel_hi:[1,1,0]
	s_nop 0
	v_pk_fma_f32 v[168:169], v[164:165], v[168:169], s[46:47] op_sel_hi:[1,1,0]
	s_nop 0
	v_pk_mul_f32 v[164:165], v[168:169], v[164:165] neg_lo:[0,1] neg_hi:[0,1]
	s_nop 0
	v_pk_fma_f32 v[164:165], v[164:165], v[166:167], 1.0 op_sel_hi:[1,1,0]
	s_nop 0
	v_bfi_b32 v153, s71, v165, v153
	v_bfi_b32 v152, s71, v164, v152
	v_cvt_f32_f16_sdwa v165, v59 dst_sel:DWORD dst_unused:UNUSED_PAD src0_sel:WORD_1
	v_cvt_f32_f16_e32 v164, v59
	v_pk_add_f32 v[152:153], v[152:153], 1.0 op_sel_hi:[1,0]
	s_nop 0
	v_pk_mul_f32 v[58:59], v[62:63], v[152:153]
	v_pk_fma_f32 v[62:63], v[164:165], v[64:65], v[154:155]
	v_pk_mul_f32 v[58:59], v[66:67], v[58:59] op_sel_hi:[0,1]
	v_pk_mul_f32 v[64:65], v[62:63], s[28:29] op_sel_hi:[1,0]
	v_cvt_pk_f16_f32 v58, v58, v59
	v_fma_f32 v59, |v64|, s74, 1.0
	v_fma_f32 v107, |v65|, s74, 1.0
	v_rcp_f32_e32 v152, v59
	v_rcp_f32_e32 v153, v107
	v_mul_f32_e64 v59, |v64|, -|v64|
	v_mul_f32_e32 v59, 0x3fb8aa3b, v59
	v_exp_f32_e32 v154, v59
	v_mul_f32_e64 v59, |v65|, -|v65|
	v_pk_fma_f32 v[164:165], v[152:153], s[40:41], v[110:111] op_sel_hi:[1,0,0]
	v_mul_f32_e32 v59, 0x3fb8aa3b, v59
	v_pk_fma_f32 v[164:165], v[152:153], v[164:165], s[42:43] op_sel_hi:[1,1,0]
	v_exp_f32_e32 v155, v59
	v_pk_fma_f32 v[164:165], v[152:153], v[164:165], s[44:45] op_sel_hi:[1,1,0]
	v_pk_mul_f32 v[62:63], v[62:63], 0.5 op_sel_hi:[1,0]
	v_pk_fma_f32 v[164:165], v[152:153], v[164:165], s[46:47] op_sel_hi:[1,1,0]
	s_nop 0
	v_pk_mul_f32 v[152:153], v[164:165], v[152:153] neg_lo:[0,1] neg_hi:[0,1]
	s_nop 0
	v_pk_fma_f32 v[152:153], v[152:153], v[154:155], 1.0 op_sel_hi:[1,1,0]
	s_nop 0
	v_bfi_b32 v65, s71, v153, v65
	v_bfi_b32 v64, s71, v152, v64
	v_cvt_f32_f16_sdwa v153, v60 dst_sel:DWORD dst_unused:UNUSED_PAD src0_sel:WORD_1
	v_cvt_f32_f16_e32 v152, v60
	v_pk_add_f32 v[64:65], v[64:65], 1.0 op_sel_hi:[1,0]
	s_nop 0
	v_pk_mul_f32 v[62:63], v[62:63], v[64:65]
	s_nop 0
	v_pk_mul_f32 v[62:63], v[66:67], v[62:63] op_sel_hi:[0,1]
	v_cvt_pk_f16_f32 v59, v62, v63
	s_waitcnt lgkmcnt(0)
	v_pk_fma_f32 v[62:63], v[152:153], v[156:157], v[160:161]
	s_waitcnt vmcnt(13)
	v_cvt_f32_f16_sdwa v161, v54 dst_sel:DWORD dst_unused:UNUSED_PAD src0_sel:WORD_1
	v_pk_mul_f32 v[64:65], v[62:63], s[28:29] op_sel_hi:[1,0]
	v_pk_mul_f32 v[62:63], v[62:63], 0.5 op_sel_hi:[1,0]
	v_fma_f32 v60, |v64|, s74, 1.0
	v_fma_f32 v107, |v65|, s74, 1.0
	v_rcp_f32_e32 v152, v60
	v_rcp_f32_e32 v153, v107
	v_mul_f32_e64 v60, |v64|, -|v64|
	v_mul_f32_e32 v60, 0x3fb8aa3b, v60
	v_exp_f32_e32 v154, v60
	v_mul_f32_e64 v60, |v65|, -|v65|
	v_pk_fma_f32 v[156:157], v[152:153], s[40:41], v[110:111] op_sel_hi:[1,0,0]
	v_mul_f32_e32 v60, 0x3fb8aa3b, v60
	v_pk_fma_f32 v[156:157], v[152:153], v[156:157], s[42:43] op_sel_hi:[1,1,0]
	v_exp_f32_e32 v155, v60
	v_pk_fma_f32 v[156:157], v[152:153], v[156:157], s[44:45] op_sel_hi:[1,1,0]
	v_cvt_f32_f16_e32 v160, v54
	v_pk_fma_f32 v[156:157], v[152:153], v[156:157], s[46:47] op_sel_hi:[1,1,0]
	s_nop 0
	v_pk_mul_f32 v[152:153], v[156:157], v[152:153] neg_lo:[0,1] neg_hi:[0,1]
	s_nop 0
	v_pk_fma_f32 v[152:153], v[152:153], v[154:155], 1.0 op_sel_hi:[1,1,0]
	s_nop 0
	v_bfi_b32 v65, s71, v153, v65
	v_bfi_b32 v64, s71, v152, v64
	v_cvt_f32_f16_sdwa v153, v61 dst_sel:DWORD dst_unused:UNUSED_PAD src0_sel:WORD_1
	v_cvt_f32_f16_e32 v152, v61
	v_pk_add_f32 v[64:65], v[64:65], 1.0 op_sel_hi:[1,0]
	s_nop 0
	v_pk_mul_f32 v[60:61], v[62:63], v[64:65]
	v_pk_fma_f32 v[62:63], v[152:153], v[158:159], v[162:163]
	v_pk_mul_f32 v[60:61], v[66:67], v[60:61] op_sel_hi:[0,1]
	v_pk_mul_f32 v[64:65], v[62:63], s[28:29] op_sel_hi:[1,0]
	v_cvt_pk_f16_f32 v60, v60, v61
	v_fma_f32 v61, |v64|, s74, 1.0
	v_fma_f32 v107, |v65|, s74, 1.0
	v_rcp_f32_e32 v152, v61
	v_rcp_f32_e32 v153, v107
	v_mul_f32_e64 v61, |v64|, -|v64|
	v_mul_f32_e32 v61, 0x3fb8aa3b, v61
	v_exp_f32_e32 v154, v61
	v_mul_f32_e64 v61, |v65|, -|v65|
	v_pk_fma_f32 v[156:157], v[152:153], s[40:41], v[110:111] op_sel_hi:[1,0,0]
	v_mul_f32_e32 v61, 0x3fb8aa3b, v61
	v_pk_fma_f32 v[156:157], v[152:153], v[156:157], s[42:43] op_sel_hi:[1,1,0]
	v_exp_f32_e32 v155, v61
	v_pk_fma_f32 v[156:157], v[152:153], v[156:157], s[44:45] op_sel_hi:[1,1,0]
	v_pk_mul_f32 v[62:63], v[62:63], 0.5 op_sel_hi:[1,0]
	v_pk_fma_f32 v[156:157], v[152:153], v[156:157], s[46:47] op_sel_hi:[1,1,0]
	s_nop 0
	v_pk_mul_f32 v[152:153], v[156:157], v[152:153] neg_lo:[0,1] neg_hi:[0,1]
	s_nop 0
	v_pk_fma_f32 v[152:153], v[152:153], v[154:155], 1.0 op_sel_hi:[1,1,0]
	s_nop 0
	v_bfi_b32 v65, s71, v153, v65
	v_bfi_b32 v64, s71, v152, v64
	v_pk_add_f32 v[64:65], v[64:65], 1.0 op_sel_hi:[1,0]
	s_nop 0
	v_pk_mul_f32 v[62:63], v[62:63], v[64:65]
	s_nop 0
	v_pk_mul_f32 v[62:63], v[66:67], v[62:63] op_sel_hi:[0,1]
	v_cvt_pk_f16_f32 v61, v62, v63
	ds_write_b128 v139, v[58:61]
	ds_read_b128 v[58:61], v119 offset:62400
	ds_read_b128 v[62:65], v119 offset:63104
	v_add_u32_e32 v66, s58, v113
	v_cmp_gt_u32_e32 vcc, s73, v66
	ds_read_b128 v[152:155], v119 offset:62416
	ds_read_b128 v[156:159], v119 offset:63120
	v_cndmask_b32_e64 v66, 0, 1.0, vcc
	s_waitcnt lgkmcnt(2)
	v_pk_fma_f32 v[58:59], v[160:161], v[58:59], v[62:63]
	s_nop 0
	v_pk_mul_f32 v[62:63], v[58:59], s[28:29] op_sel_hi:[1,0]
	v_pk_mul_f32 v[58:59], v[58:59], 0.5 op_sel_hi:[1,0]
	v_fma_f32 v54, |v62|, s74, 1.0
	v_fma_f32 v107, |v63|, s74, 1.0
	v_rcp_f32_e32 v160, v54
	v_rcp_f32_e32 v161, v107
	v_mul_f32_e64 v54, |v62|, -|v62|
	v_mul_f32_e32 v54, 0x3fb8aa3b, v54
	v_exp_f32_e32 v162, v54
	v_mul_f32_e64 v54, |v63|, -|v63|
	v_pk_fma_f32 v[164:165], v[160:161], s[40:41], v[110:111] op_sel_hi:[1,0,0]
	v_mul_f32_e32 v54, 0x3fb8aa3b, v54
	v_pk_fma_f32 v[164:165], v[160:161], v[164:165], s[42:43] op_sel_hi:[1,1,0]
	v_exp_f32_e32 v163, v54
	v_pk_fma_f32 v[164:165], v[160:161], v[164:165], s[44:45] op_sel_hi:[1,1,0]
	s_nop 0
	v_pk_fma_f32 v[164:165], v[160:161], v[164:165], s[46:47] op_sel_hi:[1,1,0]
	s_nop 0
	v_pk_mul_f32 v[160:161], v[164:165], v[160:161] neg_lo:[0,1] neg_hi:[0,1]
	s_nop 0
	v_pk_fma_f32 v[160:161], v[160:161], v[162:163], 1.0 op_sel_hi:[1,1,0]
	s_nop 0
	v_bfi_b32 v63, s71, v161, v63
	v_bfi_b32 v62, s71, v160, v62
	v_cvt_f32_f16_sdwa v161, v55 dst_sel:DWORD dst_unused:UNUSED_PAD src0_sel:WORD_1
	v_cvt_f32_f16_e32 v160, v55
	v_pk_add_f32 v[62:63], v[62:63], 1.0 op_sel_hi:[1,0]
	s_nop 0
	v_pk_mul_f32 v[54:55], v[58:59], v[62:63]
	v_pk_fma_f32 v[58:59], v[160:161], v[60:61], v[64:65]
	v_pk_mul_f32 v[54:55], v[66:67], v[54:55] op_sel_hi:[0,1]
	v_pk_mul_f32 v[60:61], v[58:59], s[28:29] op_sel_hi:[1,0]
	v_cvt_pk_f16_f32 v54, v54, v55
	v_fma_f32 v55, |v60|, s74, 1.0
	v_fma_f32 v63, |v61|, s74, 1.0
	v_rcp_f32_e32 v62, v55
	v_rcp_f32_e32 v63, v63
	v_mul_f32_e64 v55, |v60|, -|v60|
	v_mul_f32_e32 v55, 0x3fb8aa3b, v55
	v_exp_f32_e32 v64, v55
	v_mul_f32_e64 v55, |v61|, -|v61|
	v_pk_fma_f32 v[160:161], v[62:63], s[40:41], v[110:111] op_sel_hi:[1,0,0]
	v_mul_f32_e32 v55, 0x3fb8aa3b, v55
	v_pk_fma_f32 v[160:161], v[62:63], v[160:161], s[42:43] op_sel_hi:[1,1,0]
	v_exp_f32_e32 v65, v55
	v_pk_fma_f32 v[160:161], v[62:63], v[160:161], s[44:45] op_sel_hi:[1,1,0]
	v_pk_mul_f32 v[58:59], v[58:59], 0.5 op_sel_hi:[1,0]
	v_pk_fma_f32 v[160:161], v[62:63], v[160:161], s[46:47] op_sel_hi:[1,1,0]
	s_nop 0
	v_pk_mul_f32 v[62:63], v[160:161], v[62:63] neg_lo:[0,1] neg_hi:[0,1]
	s_nop 0
	v_pk_fma_f32 v[62:63], v[62:63], v[64:65], 1.0 op_sel_hi:[1,1,0]
	s_nop 0
	v_bfi_b32 v61, s71, v63, v61
	v_bfi_b32 v60, s71, v62, v60
	v_cvt_f32_f16_sdwa v63, v56 dst_sel:DWORD dst_unused:UNUSED_PAD src0_sel:WORD_1
	v_cvt_f32_f16_e32 v62, v56
	v_pk_add_f32 v[60:61], v[60:61], 1.0 op_sel_hi:[1,0]
	s_nop 0
	v_pk_mul_f32 v[58:59], v[58:59], v[60:61]
	s_nop 0
	v_pk_mul_f32 v[58:59], v[66:67], v[58:59] op_sel_hi:[0,1]
	v_cvt_pk_f16_f32 v55, v58, v59
	s_waitcnt lgkmcnt(0)
	v_pk_fma_f32 v[58:59], v[62:63], v[152:153], v[156:157]
	s_nop 0
	v_pk_mul_f32 v[60:61], v[58:59], s[28:29] op_sel_hi:[1,0]
	v_pk_mul_f32 v[58:59], v[58:59], 0.5 op_sel_hi:[1,0]
	v_fma_f32 v56, |v60|, s74, 1.0
	v_fma_f32 v63, |v61|, s74, 1.0
	v_rcp_f32_e32 v62, v56
	v_rcp_f32_e32 v63, v63
	v_mul_f32_e64 v56, |v60|, -|v60|
	v_mul_f32_e32 v56, 0x3fb8aa3b, v56
	v_exp_f32_e32 v64, v56
	v_mul_f32_e64 v56, |v61|, -|v61|
	v_pk_fma_f32 v[152:153], v[62:63], s[40:41], v[110:111] op_sel_hi:[1,0,0]
	v_mul_f32_e32 v56, 0x3fb8aa3b, v56
	v_pk_fma_f32 v[152:153], v[62:63], v[152:153], s[42:43] op_sel_hi:[1,1,0]
	v_exp_f32_e32 v65, v56
	v_pk_fma_f32 v[152:153], v[62:63], v[152:153], s[44:45] op_sel_hi:[1,1,0]
	s_nop 0
	v_pk_fma_f32 v[152:153], v[62:63], v[152:153], s[46:47] op_sel_hi:[1,1,0]
	s_nop 0
	v_pk_mul_f32 v[62:63], v[152:153], v[62:63] neg_lo:[0,1] neg_hi:[0,1]
	s_nop 0
	v_pk_fma_f32 v[62:63], v[62:63], v[64:65], 1.0 op_sel_hi:[1,1,0]
	s_nop 0
	v_bfi_b32 v61, s71, v63, v61
	v_bfi_b32 v60, s71, v62, v60
	v_cvt_f32_f16_sdwa v63, v57 dst_sel:DWORD dst_unused:UNUSED_PAD src0_sel:WORD_1
	v_cvt_f32_f16_e32 v62, v57
	v_pk_add_f32 v[60:61], v[60:61], 1.0 op_sel_hi:[1,0]
	s_nop 0
	v_pk_mul_f32 v[56:57], v[58:59], v[60:61]
	v_pk_fma_f32 v[58:59], v[62:63], v[154:155], v[158:159]
	v_pk_mul_f32 v[56:57], v[66:67], v[56:57] op_sel_hi:[0,1]
	v_pk_mul_f32 v[60:61], v[58:59], s[28:29] op_sel_hi:[1,0]
	v_cvt_pk_f16_f32 v56, v56, v57
	v_fma_f32 v57, |v60|, s74, 1.0
	v_fma_f32 v63, |v61|, s74, 1.0
	v_rcp_f32_e32 v62, v57
	v_rcp_f32_e32 v63, v63
	v_mul_f32_e64 v57, |v60|, -|v60|
	v_mul_f32_e32 v57, 0x3fb8aa3b, v57
	v_exp_f32_e32 v64, v57
	v_mul_f32_e64 v57, |v61|, -|v61|
	v_pk_fma_f32 v[110:111], v[62:63], s[40:41], v[110:111] op_sel_hi:[1,0,0]
	v_mul_f32_e32 v57, 0x3fb8aa3b, v57
	v_pk_fma_f32 v[110:111], v[62:63], v[110:111], s[42:43] op_sel_hi:[1,1,0]
	v_exp_f32_e32 v65, v57
	v_pk_fma_f32 v[110:111], v[62:63], v[110:111], s[44:45] op_sel_hi:[1,1,0]
	v_pk_mul_f32 v[58:59], v[58:59], 0.5 op_sel_hi:[1,0]
	v_pk_fma_f32 v[110:111], v[62:63], v[110:111], s[46:47] op_sel_hi:[1,1,0]
	s_nop 0
	v_pk_mul_f32 v[62:63], v[110:111], v[62:63] neg_lo:[0,1] neg_hi:[0,1]
	s_nop 0
	v_pk_fma_f32 v[62:63], v[62:63], v[64:65], 1.0 op_sel_hi:[1,1,0]
	s_nop 0
	v_bfi_b32 v61, s71, v63, v61
	v_bfi_b32 v60, s71, v62, v60
	v_pk_add_f32 v[60:61], v[60:61], 1.0 op_sel_hi:[1,0]
	s_nop 0
	v_pk_mul_f32 v[58:59], v[58:59], v[60:61]
	s_nop 0
	v_pk_mul_f32 v[58:59], v[66:67], v[58:59] op_sel_hi:[0,1]
	v_cvt_pk_f16_f32 v57, v58, v59
	ds_write_b128 v140, v[54:57]
	s_and_saveexec_b64 s[20:21], s[12:13]
	s_cbranch_execnz .LBB3_36
	s_or_b64 exec, exec, s[20:21]
	s_and_saveexec_b64 s[20:21], s[14:15]
	s_cbranch_execnz .LBB3_37

.LBB3_11:
	s_waitcnt vmcnt(11)
	ds_read_b128 v[46:49], v122 offset:62400
	ds_read_b128 v[50:53], v122 offset:63104
	s_waitcnt vmcnt(10)
	v_cvt_f32_f16_sdwa v63, v42 dst_sel:DWORD dst_unused:UNUSED_PAD src0_sel:WORD_1
	v_cvt_f32_f16_e32 v62, v42
	v_mov_b64_e32 v[152:153], s[34:35]
	v_add_u32_e32 v54, s58, v116
	v_cmp_gt_u32_e32 vcc, s73, v54
	s_waitcnt lgkmcnt(0)
	v_pk_fma_f32 v[46:47], v[62:63], v[46:47], v[50:51]
	ds_read_b128 v[54:57], v122 offset:62416
	ds_read_b128 v[58:61], v122 offset:63120
	v_pk_mul_f32 v[50:51], v[46:47], s[28:29] op_sel_hi:[1,0]
	v_pk_mul_f32 v[46:47], v[46:47], 0.5 op_sel_hi:[1,0]
	v_fma_f32 v42, |v50|, s74, 1.0
	v_fma_f32 v63, |v51|, s74, 1.0
	v_rcp_f32_e32 v62, v42
	v_rcp_f32_e32 v63, v63
	v_mul_f32_e64 v42, |v50|, -|v50|
	v_mul_f32_e32 v42, 0x3fb8aa3b, v42
	v_exp_f32_e32 v110, v42
	v_mul_f32_e64 v42, |v51|, -|v51|
	v_pk_fma_f32 v[154:155], v[62:63], s[40:41], v[152:153] op_sel_hi:[1,0,0]
	v_mul_f32_e32 v42, 0x3fb8aa3b, v42
	v_pk_fma_f32 v[154:155], v[62:63], v[154:155], s[42:43] op_sel_hi:[1,1,0]
	v_exp_f32_e32 v111, v42
	v_pk_fma_f32 v[154:155], v[62:63], v[154:155], s[44:45] op_sel_hi:[1,1,0]
	v_cndmask_b32_e64 v64, 0, 1.0, vcc
	v_pk_fma_f32 v[154:155], v[62:63], v[154:155], s[46:47] op_sel_hi:[1,1,0]
	s_nop 0
	v_pk_mul_f32 v[62:63], v[154:155], v[62:63] neg_lo:[0,1] neg_hi:[0,1]
	s_nop 0
	v_pk_fma_f32 v[62:63], v[62:63], v[110:111], 1.0 op_sel_hi:[1,1,0]
	s_nop 0
	v_bfi_b32 v51, s71, v63, v51
	v_bfi_b32 v50, s71, v62, v50
	v_cvt_f32_f16_sdwa v63, v43 dst_sel:DWORD dst_unused:UNUSED_PAD src0_sel:WORD_1
	v_cvt_f32_f16_e32 v62, v43
	v_pk_add_f32 v[50:51], v[50:51], 1.0 op_sel_hi:[1,0]
	s_nop 0
	v_pk_mul_f32 v[42:43], v[46:47], v[50:51]
	v_pk_fma_f32 v[46:47], v[62:63], v[48:49], v[52:53]
	v_pk_mul_f32 v[42:43], v[64:65], v[42:43] op_sel_hi:[0,1]
	v_pk_mul_f32 v[48:49], v[46:47], s[28:29] op_sel_hi:[1,0]
	v_cvt_pk_f16_f32 v42, v42, v43
	v_fma_f32 v43, |v48|, s74, 1.0
	v_fma_f32 v51, |v49|, s74, 1.0
	v_rcp_f32_e32 v50, v43
	v_rcp_f32_e32 v51, v51
	v_mul_f32_e64 v43, |v48|, -|v48|
	v_mul_f32_e32 v43, 0x3fb8aa3b, v43
	v_exp_f32_e32 v52, v43
	v_mul_f32_e64 v43, |v49|, -|v49|
	v_pk_fma_f32 v[62:63], v[50:51], s[40:41], v[152:153] op_sel_hi:[1,0,0]
	v_mul_f32_e32 v43, 0x3fb8aa3b, v43
	v_pk_fma_f32 v[62:63], v[50:51], v[62:63], s[42:43] op_sel_hi:[1,1,0]
	v_exp_f32_e32 v53, v43
	v_pk_fma_f32 v[62:63], v[50:51], v[62:63], s[44:45] op_sel_hi:[1,1,0]
	v_pk_mul_f32 v[46:47], v[46:47], 0.5 op_sel_hi:[1,0]
	v_pk_fma_f32 v[62:63], v[50:51], v[62:63], s[46:47] op_sel_hi:[1,1,0]
	s_nop 0
	v_pk_mul_f32 v[50:51], v[62:63], v[50:51] neg_lo:[0,1] neg_hi:[0,1]
	s_nop 0
	v_pk_fma_f32 v[50:51], v[50:51], v[52:53], 1.0 op_sel_hi:[1,1,0]
	s_nop 0
	v_bfi_b32 v49, s71, v51, v49
	v_bfi_b32 v48, s71, v50, v48
	v_cvt_f32_f16_sdwa v51, v44 dst_sel:DWORD dst_unused:UNUSED_PAD src0_sel:WORD_1
	v_cvt_f32_f16_e32 v50, v44
	v_pk_add_f32 v[48:49], v[48:49], 1.0 op_sel_hi:[1,0]
	s_nop 0
	v_pk_mul_f32 v[46:47], v[46:47], v[48:49]
	s_nop 0
	v_pk_mul_f32 v[46:47], v[64:65], v[46:47] op_sel_hi:[0,1]
	v_cvt_pk_f16_f32 v43, v46, v47
	s_waitcnt lgkmcnt(0)
	v_pk_fma_f32 v[46:47], v[50:51], v[54:55], v[58:59]
	s_nop 0
	v_pk_mul_f32 v[48:49], v[46:47], s[28:29] op_sel_hi:[1,0]
	v_pk_mul_f32 v[46:47], v[46:47], 0.5 op_sel_hi:[1,0]
	v_fma_f32 v44, |v48|, s74, 1.0
	v_fma_f32 v51, |v49|, s74, 1.0
	v_rcp_f32_e32 v50, v44
	v_rcp_f32_e32 v51, v51
	v_mul_f32_e64 v44, |v48|, -|v48|
	v_mul_f32_e32 v44, 0x3fb8aa3b, v44
	v_exp_f32_e32 v52, v44
	v_mul_f32_e64 v44, |v49|, -|v49|
	v_pk_fma_f32 v[54:55], v[50:51], s[40:41], v[152:153] op_sel_hi:[1,0,0]
	v_mul_f32_e32 v44, 0x3fb8aa3b, v44
	v_pk_fma_f32 v[54:55], v[50:51], v[54:55], s[42:43] op_sel_hi:[1,1,0]
	v_exp_f32_e32 v53, v44
	v_pk_fma_f32 v[54:55], v[50:51], v[54:55], s[44:45] op_sel_hi:[1,1,0]
	s_nop 0
	v_pk_fma_f32 v[54:55], v[50:51], v[54:55], s[46:47] op_sel_hi:[1,1,0]
	s_nop 0
	v_pk_mul_f32 v[50:51], v[54:55], v[50:51] neg_lo:[0,1] neg_hi:[0,1]
	s_nop 0
	v_pk_fma_f32 v[50:51], v[50:51], v[52:53], 1.0 op_sel_hi:[1,1,0]
	s_nop 0
	v_bfi_b32 v49, s71, v51, v49
	v_bfi_b32 v48, s71, v50, v48
	v_cvt_f32_f16_sdwa v51, v45 dst_sel:DWORD dst_unused:UNUSED_PAD src0_sel:WORD_1
	v_cvt_f32_f16_e32 v50, v45
	v_pk_add_f32 v[48:49], v[48:49], 1.0 op_sel_hi:[1,0]
	s_nop 0
	v_pk_mul_f32 v[44:45], v[46:47], v[48:49]
	v_pk_fma_f32 v[46:47], v[50:51], v[56:57], v[60:61]
	v_pk_mul_f32 v[44:45], v[64:65], v[44:45] op_sel_hi:[0,1]
	v_pk_mul_f32 v[48:49], v[46:47], s[28:29] op_sel_hi:[1,0]
	v_cvt_pk_f16_f32 v44, v44, v45
	v_fma_f32 v45, |v48|, s74, 1.0
	v_fma_f32 v51, |v49|, s74, 1.0
	v_rcp_f32_e32 v50, v45
	v_rcp_f32_e32 v51, v51
	v_mul_f32_e64 v45, |v48|, -|v48|
	v_mul_f32_e32 v45, 0x3fb8aa3b, v45
	v_exp_f32_e32 v52, v45
	v_mul_f32_e64 v45, |v49|, -|v49|
	v_pk_fma_f32 v[54:55], v[50:51], s[40:41], v[152:153] op_sel_hi:[1,0,0]
	v_mul_f32_e32 v45, 0x3fb8aa3b, v45
	v_pk_fma_f32 v[54:55], v[50:51], v[54:55], s[42:43] op_sel_hi:[1,1,0]
	v_exp_f32_e32 v53, v45
	v_pk_fma_f32 v[54:55], v[50:51], v[54:55], s[44:45] op_sel_hi:[1,1,0]
	v_pk_mul_f32 v[46:47], v[46:47], 0.5 op_sel_hi:[1,0]
	v_pk_fma_f32 v[54:55], v[50:51], v[54:55], s[46:47] op_sel_hi:[1,1,0]
	s_nop 0
	v_pk_mul_f32 v[50:51], v[54:55], v[50:51] neg_lo:[0,1] neg_hi:[0,1]
	s_nop 0
	v_pk_fma_f32 v[50:51], v[50:51], v[52:53], 1.0 op_sel_hi:[1,1,0]
	s_nop 0
	v_bfi_b32 v49, s71, v51, v49
	v_bfi_b32 v48, s71, v50, v48
	v_pk_add_f32 v[48:49], v[48:49], 1.0 op_sel_hi:[1,0]
	s_nop 0
	v_pk_mul_f32 v[46:47], v[46:47], v[48:49]
	s_nop 0
	v_pk_mul_f32 v[46:47], v[64:65], v[46:47] op_sel_hi:[0,1]
	v_cvt_pk_f16_f32 v45, v46, v47
	ds_write_b128 v143, v[42:45]
.LBB3_12:
	s_or_b64 exec, exec, s[20:21]
	v_mov_b32_e32 v107, v67
	s_waitcnt vmcnt(5)
	ds_write_b128 v123, v[22:25] offset:35776
	ds_write_b128 v124, v[26:29] offset:40896
	ds_write_b128 v125, v[30:33] offset:46016
	ds_write_b128 v126, v[34:37] offset:51136
	ds_write_b128 v127, v[38:41] offset:56256
	v_lshl_add_u64 v[22:23], s[56:57], 0, v[106:107]
	v_add_co_u32_e32 v24, vcc, 0xc000, v22
	s_waitcnt lgkmcnt(0)
	s_nop 0
	v_addc_co_u32_e32 v25, vcc, 0, v23, vcc
	v_add_co_u32_e32 v28, vcc, 0xd000, v22
	s_barrier
	v_add_u32_e32 v196, 0x6f80, v129
	v_add_u32_e32 v197, 0x6f80, v123
	v_add_u32_e32 v198, 0x6f80, v124
	v_add_u32_e32 v199, 0x6f80, v125
	v_add_u32_e32 v200, 0x6f80, v126
	v_add_u32_e32 v201, 0x6f80, v127
	s_nop 0
	v_addc_co_u32_e32 v29, vcc, 0, v23, vcc
	v_add_co_u32_e32 v32, vcc, 0xf000, v22
	s_nop 1
	v_addc_co_u32_e32 v33, vcc, 0, v23, vcc
	v_add_co_u32_e32 v36, vcc, 0x10000, v22
	global_load_dwordx4 v[24:27], v[24:25], off offset:2048
	s_nop 0
	global_load_dwordx4 v[28:31], v[28:29], off offset:3072
	v_addc_co_u32_e32 v37, vcc, 0, v23, vcc
	v_add_co_u32_e32 v40, vcc, 0x11000, v22
	global_load_dwordx4 v[32:35], v[32:33], off
	s_nop 0
	global_load_dwordx4 v[36:39], v[36:37], off offset:1024
	v_addc_co_u32_e32 v41, vcc, 0, v23, vcc
	global_load_dwordx4 v[40:43], v[40:41], off offset:2048
	s_waitcnt vmcnt(5)
	ds_write_b128 v197, v[2:5] offset:35776
	ds_write_b128 v198, v[6:9] offset:40896
	ds_write_b128 v199, v[10:13] offset:46016
	ds_write_b128 v200, v[14:17] offset:51136
	ds_write_b128 v201, v[18:21] offset:56256
	s_waitcnt vmcnt(5)
	ds_read_b128 v[44:47], v129 offset:35776
	ds_read_b128 v[48:51], v144
	ds_read_b128 v[52:55], v144 offset:64
	ds_read_b128 v[56:59], v129 offset:35840
	ds_read_b128 v[60:63], v129 offset:42432
	ds_read_b128 v[152:155], v129 offset:42496
	ds_read_b128 v[156:159], v129 offset:49088
	ds_read_b128 v[160:163], v129 offset:49152
	s_waitcnt lgkmcnt(6)
	v_mfma_f32_16x16x32_f16 v[44:47], v[44:47], v[48:51], 0
	ds_read_b128 v[164:167], v129 offset:55744
	ds_read_b128 v[168:171], v129 offset:55808
	s_waitcnt lgkmcnt(5)
	v_mfma_f32_16x16x32_f16 v[60:63], v[60:63], v[48:51], 0
	v_mfma_f32_16x16x32_f16 v[44:47], v[56:59], v[52:55], v[44:47]
	s_waitcnt lgkmcnt(4)
	v_mfma_f32_16x16x32_f16 v[56:59], v[152:155], v[52:55], v[60:63]
	ds_read_b128 v[152:155], v129 offset:35904
	s_waitcnt lgkmcnt(4)
	v_mfma_f32_16x16x32_f16 v[156:159], v[156:159], v[48:51], 0
	s_waitcnt lgkmcnt(2)
	v_mfma_f32_16x16x32_f16 v[48:51], v[164:167], v[48:51], 0
	v_mfma_f32_16x16x32_f16 v[60:63], v[160:163], v[52:55], v[156:159]
	s_waitcnt lgkmcnt(1)
	v_mfma_f32_16x16x32_f16 v[48:51], v[168:171], v[52:55], v[48:51]
	ds_read_b128 v[52:55], v144 offset:128
	s_nop 1
	ds_read_b128 v[156:159], v144 offset:192
	ds_read_b128 v[160:163], v129 offset:35968
	s_waitcnt lgkmcnt(2)
	v_mfma_f32_16x16x32_f16 v[44:47], v[152:155], v[52:55], v[44:47]
	ds_read_b128 v[152:155], v129 offset:42560
	ds_read_b128 v[164:167], v129 offset:42624
	s_waitcnt lgkmcnt(1)
	v_mfma_f32_16x16x32_f16 v[56:59], v[152:155], v[52:55], v[56:59]
	ds_read_b128 v[152:155], v129 offset:49216
	ds_read_b128 v[168:171], v129 offset:49280
	s_waitcnt lgkmcnt(1)
	v_mfma_f32_16x16x32_f16 v[60:63], v[152:155], v[52:55], v[60:63]
	ds_read_b128 v[152:155], v129 offset:55872
	ds_read_b128 v[172:175], v129 offset:55936
	s_waitcnt lgkmcnt(1)
	v_mfma_f32_16x16x32_f16 v[48:51], v[152:155], v[52:55], v[48:51]
	v_mfma_f32_16x16x32_f16 v[44:47], v[160:163], v[156:159], v[44:47]
	ds_read_b128 v[52:55], v144 offset:256
	ds_read_b128 v[152:155], v144 offset:320
	ds_read_b128 v[160:163], v129 offset:36032
	ds_read_b128 v[176:179], v129 offset:36096
	v_mfma_f32_16x16x32_f16 v[56:59], v[164:167], v[156:159], v[56:59]
	ds_read_b128 v[164:167], v129 offset:42688
	ds_read_b128 v[180:183], v129 offset:42752
	ds_read_b128 v[184:187], v129 offset:49344
	ds_read_b128 v[188:191], v129 offset:49408
	v_mfma_f32_16x16x32_f16 v[60:63], v[168:171], v[156:159], v[60:63]
	ds_read_b128 v[168:171], v129 offset:56000
	ds_read_b128 v[192:195], v129 offset:56064
	s_waitcnt lgkmcnt(0)
	v_mfma_f32_16x16x32_f16 v[48:51], v[172:175], v[156:159], v[48:51]
	v_add_co_u32_e32 v18, vcc, s75, v22
	v_mfma_f32_16x16x32_f16 v[2:5], v[160:163], v[52:55], v[44:47]
	s_nop 0
	v_addc_co_u32_e32 v19, vcc, 0, v23, vcc
	s_waitcnt lgkmcnt(0)
	v_add_co_u32_e32 v44, vcc, s76, v22
	v_mfma_f32_16x16x32_f16 v[14:17], v[168:171], v[52:55], v[48:51]
	s_nop 0
	v_addc_co_u32_e32 v45, vcc, 0, v23, vcc
	s_barrier
	v_add_co_u32_e32 v48, vcc, s77, v22
	v_mfma_f32_16x16x32_f16 v[6:9], v[164:167], v[52:55], v[56:59]
	s_nop 0
	v_addc_co_u32_e32 v49, vcc, 0, v23, vcc
	v_mfma_f32_16x16x32_f16 v[10:13], v[184:187], v[52:55], v[60:63]
	v_add_co_u32_e32 v52, vcc, s78, v22
	global_load_dwordx4 v[18:21], v[18:19], off offset:3072
	s_nop 0
	global_load_dwordx4 v[44:47], v[44:45], off
	v_addc_co_u32_e32 v53, vcc, 0, v23, vcc
	v_add_co_u32_e32 v56, vcc, s79, v22
	global_load_dwordx4 v[48:51], v[48:49], off offset:1024
	s_nop 0
	global_load_dwordx4 v[52:55], v[52:53], off offset:2048
	v_addc_co_u32_e32 v57, vcc, 0, v23, vcc
	global_load_dwordx4 v[56:59], v[56:57], off offset:3072
	s_waitcnt vmcnt(9)
	ds_write_b128 v123, v[24:27] offset:35776
	s_waitcnt vmcnt(8)
	ds_write_b128 v124, v[28:31] offset:40896
	s_waitcnt vmcnt(7)
	ds_write_b128 v125, v[32:35] offset:46016
	s_waitcnt vmcnt(6)
	ds_write_b128 v126, v[36:39] offset:51136
	s_waitcnt vmcnt(5)
	ds_write_b128 v127, v[40:43] offset:56256
	v_mfma_f32_16x16x32_f16 v[2:5], v[176:179], v[152:155], v[2:5]
	v_mfma_f32_16x16x32_f16 v[6:9], v[180:183], v[152:155], v[6:9]
	v_mfma_f32_16x16x32_f16 v[10:13], v[188:191], v[152:155], v[10:13]
	v_mfma_f32_16x16x32_f16 v[14:17], v[192:195], v[152:155], v[14:17]
	ds_read_b128 v[60:63], v196 offset:35776
	ds_read_b128 v[152:155], v144 offset:416
	ds_read_b128 v[208:211], v196 offset:42432
	ds_read_b128 v[212:215], v196 offset:49088
	ds_read_b128 v[216:219], v196 offset:55744
	ds_read_b128 v[156:159], v144 offset:480
	ds_read_b128 v[160:163], v196 offset:35840
	ds_read_b128 v[164:167], v196 offset:42496
	ds_read_b128 v[168:171], v196 offset:49152
	ds_read_b128 v[172:175], v196 offset:55808
	s_waitcnt lgkmcnt(8)
	v_mfma_f32_16x16x32_f16 v[2:5], v[60:63], v[152:155], v[2:5]
	s_waitcnt lgkmcnt(7)
	v_mfma_f32_16x16x32_f16 v[6:9], v[208:211], v[152:155], v[6:9]
	s_waitcnt lgkmcnt(6)
	v_mfma_f32_16x16x32_f16 v[10:13], v[212:215], v[152:155], v[10:13]
	s_waitcnt lgkmcnt(5)
	v_mfma_f32_16x16x32_f16 v[14:17], v[216:219], v[152:155], v[14:17]
	s_waitcnt lgkmcnt(0)
	ds_read_b128 v[60:63], v196 offset:35904
	v_mfma_f32_16x16x32_f16 v[2:5], v[160:163], v[156:159], v[2:5]
	v_mfma_f32_16x16x32_f16 v[6:9], v[164:167], v[156:159], v[6:9]
	v_mfma_f32_16x16x32_f16 v[10:13], v[168:171], v[156:159], v[10:13]
	s_waitcnt lgkmcnt(1)
	v_mfma_f32_16x16x32_f16 v[14:17], v[172:175], v[156:159], v[14:17]
	ds_read_b128 v[152:155], v144 offset:544
	ds_read_b128 v[208:211], v196 offset:42560
	ds_read_b128 v[212:215], v196 offset:49216
	ds_read_b128 v[216:219], v196 offset:55872
	ds_read_b128 v[156:159], v144 offset:608
	ds_read_b128 v[160:163], v196 offset:35968
	ds_read_b128 v[164:167], v196 offset:42624
	ds_read_b128 v[168:171], v196 offset:49280
	ds_read_b128 v[172:175], v196 offset:55936
	s_waitcnt lgkmcnt(8)
	v_mfma_f32_16x16x32_f16 v[2:5], v[60:63], v[152:155], v[2:5]
	s_waitcnt lgkmcnt(7)
	v_mfma_f32_16x16x32_f16 v[6:9], v[208:211], v[152:155], v[6:9]
	s_waitcnt lgkmcnt(6)
	v_mfma_f32_16x16x32_f16 v[10:13], v[212:215], v[152:155], v[10:13]
	s_waitcnt lgkmcnt(5)
	v_mfma_f32_16x16x32_f16 v[14:17], v[216:219], v[152:155], v[14:17]
	s_waitcnt lgkmcnt(0)
	v_mfma_f32_16x16x32_f16 v[2:5], v[160:163], v[156:159], v[2:5]
	ds_read_b128 v[60:63], v144 offset:672
	ds_read_b128 v[152:155], v144 offset:736
	ds_read_b128 v[160:163], v196 offset:36032
	ds_read_b128 v[176:179], v196 offset:36096
	v_mfma_f32_16x16x32_f16 v[6:9], v[164:167], v[156:159], v[6:9]
	ds_read_b128 v[164:167], v196 offset:42688
	ds_read_b128 v[180:183], v196 offset:42752
	ds_read_b128 v[184:187], v196 offset:49344
	ds_read_b128 v[188:191], v196 offset:49408
	v_mfma_f32_16x16x32_f16 v[10:13], v[168:171], v[156:159], v[10:13]
	ds_read_b128 v[168:171], v196 offset:56000
	ds_read_b128 v[192:195], v196 offset:56064
	s_waitcnt lgkmcnt(0)
	v_add_co_u32_e32 v24, vcc, s80, v22
	v_addc_co_u32_e32 v25, vcc, 0, v23, vcc
	v_add_co_u32_e32 v28, vcc, s81, v22
	s_waitcnt lgkmcnt(0)
	s_nop 0
	v_addc_co_u32_e32 v29, vcc, 0, v23, vcc
	v_add_co_u32_e32 v32, vcc, s82, v22
	s_barrier
	s_nop 0
	v_addc_co_u32_e32 v33, vcc, 0, v23, vcc
	v_add_co_u32_e32 v36, vcc, s83, v22
	s_nop 1
	v_addc_co_u32_e32 v37, vcc, 0, v23, vcc
	v_add_co_u32_e32 v40, vcc, s84, v22
	global_load_dwordx4 v[24:27], v[24:25], off
	s_nop 0
	global_load_dwordx4 v[28:31], v[28:29], off offset:1024
	s_nop 0
	global_load_dwordx4 v[32:35], v[32:33], off offset:2048
	s_nop 0
	global_load_dwordx4 v[36:39], v[36:37], off offset:3072
	v_addc_co_u32_e32 v41, vcc, 0, v23, vcc
	global_load_dwordx4 v[40:43], v[40:41], off
	s_waitcnt vmcnt(9)
	ds_write_b128 v197, v[18:21] offset:35776
	s_waitcnt vmcnt(8)
	ds_write_b128 v198, v[44:47] offset:40896
	s_waitcnt vmcnt(7)
	ds_write_b128 v199, v[48:51] offset:46016
	s_waitcnt vmcnt(6)
	ds_write_b128 v200, v[52:55] offset:51136
	s_waitcnt vmcnt(5)
	ds_write_b128 v201, v[56:59] offset:56256
	v_mfma_f32_16x16x32_f16 v[14:17], v[172:175], v[156:159], v[14:17]
	v_mfma_f32_16x16x32_f16 v[2:5], v[160:163], v[60:63], v[2:5]
	v_mfma_f32_16x16x32_f16 v[6:9], v[164:167], v[60:63], v[6:9]
	v_mfma_f32_16x16x32_f16 v[10:13], v[184:187], v[60:63], v[10:13]
	v_mfma_f32_16x16x32_f16 v[14:17], v[168:171], v[60:63], v[14:17]
	v_mfma_f32_16x16x32_f16 v[2:5], v[176:179], v[152:155], v[2:5]
	v_mfma_f32_16x16x32_f16 v[6:9], v[180:183], v[152:155], v[6:9]
	v_mfma_f32_16x16x32_f16 v[10:13], v[188:191], v[152:155], v[10:13]
	v_mfma_f32_16x16x32_f16 v[14:17], v[192:195], v[152:155], v[14:17]
	ds_read_b128 v[60:63], v129 offset:35776
	ds_read_b128 v[152:155], v144 offset:832
	ds_read_b128 v[208:211], v129 offset:42432
	ds_read_b128 v[212:215], v129 offset:49088
	ds_read_b128 v[216:219], v129 offset:55744
	ds_read_b128 v[156:159], v144 offset:896
	ds_read_b128 v[160:163], v129 offset:35840
	ds_read_b128 v[164:167], v129 offset:42496
	ds_read_b128 v[168:171], v129 offset:49152
	ds_read_b128 v[172:175], v129 offset:55808
	s_waitcnt lgkmcnt(8)
	v_mfma_f32_16x16x32_f16 v[2:5], v[60:63], v[152:155], v[2:5]
	s_waitcnt lgkmcnt(7)
	v_mfma_f32_16x16x32_f16 v[6:9], v[208:211], v[152:155], v[6:9]
	s_waitcnt lgkmcnt(6)
	v_mfma_f32_16x16x32_f16 v[10:13], v[212:215], v[152:155], v[10:13]
	s_waitcnt lgkmcnt(5)
	v_mfma_f32_16x16x32_f16 v[14:17], v[216:219], v[152:155], v[14:17]
	s_waitcnt lgkmcnt(0)
	ds_read_b128 v[60:63], v129 offset:35904
	v_mfma_f32_16x16x32_f16 v[2:5], v[160:163], v[156:159], v[2:5]
	v_mfma_f32_16x16x32_f16 v[6:9], v[164:167], v[156:159], v[6:9]
	v_mfma_f32_16x16x32_f16 v[10:13], v[168:171], v[156:159], v[10:13]
	s_waitcnt lgkmcnt(1)
	v_mfma_f32_16x16x32_f16 v[14:17], v[172:175], v[156:159], v[14:17]
	ds_read_b128 v[152:155], v144 offset:960
	ds_read_b128 v[208:211], v129 offset:42560
	ds_read_b128 v[212:215], v129 offset:49216
	ds_read_b128 v[216:219], v129 offset:55872
	ds_read_b128 v[156:159], v144 offset:1024
	ds_read_b128 v[160:163], v129 offset:35968
	ds_read_b128 v[164:167], v129 offset:42624
	ds_read_b128 v[168:171], v129 offset:49280
	ds_read_b128 v[172:175], v129 offset:55936
	s_waitcnt lgkmcnt(8)
	v_mfma_f32_16x16x32_f16 v[2:5], v[60:63], v[152:155], v[2:5]
	s_waitcnt lgkmcnt(7)
	v_mfma_f32_16x16x32_f16 v[6:9], v[208:211], v[152:155], v[6:9]
	s_waitcnt lgkmcnt(6)
	v_mfma_f32_16x16x32_f16 v[10:13], v[212:215], v[152:155], v[10:13]
	s_waitcnt lgkmcnt(5)
	v_mfma_f32_16x16x32_f16 v[14:17], v[216:219], v[152:155], v[14:17]
	s_waitcnt lgkmcnt(0)
	v_mfma_f32_16x16x32_f16 v[2:5], v[160:163], v[156:159], v[2:5]
	ds_read_b128 v[60:63], v144 offset:1088
	ds_read_b128 v[152:155], v144 offset:1152
	ds_read_b128 v[160:163], v129 offset:36032
	ds_read_b128 v[176:179], v129 offset:36096
	v_mfma_f32_16x16x32_f16 v[6:9], v[164:167], v[156:159], v[6:9]
	ds_read_b128 v[164:167], v129 offset:42688
	ds_read_b128 v[180:183], v129 offset:42752
	ds_read_b128 v[184:187], v129 offset:49344
	ds_read_b128 v[188:191], v129 offset:49408
	v_mfma_f32_16x16x32_f16 v[10:13], v[168:171], v[156:159], v[10:13]
	ds_read_b128 v[168:171], v129 offset:56000
	ds_read_b128 v[192:195], v129 offset:56064
	s_waitcnt lgkmcnt(0)
	v_add_co_u32_e32 v18, vcc, s85, v22
	v_addc_co_u32_e32 v19, vcc, 0, v23, vcc
	v_add_co_u32_e32 v44, vcc, s27, v22
	s_waitcnt lgkmcnt(0)
	s_nop 0
	v_addc_co_u32_e32 v45, vcc, 0, v23, vcc
	v_add_co_u32_e32 v48, vcc, s86, v22
	s_barrier
	s_nop 0
	v_addc_co_u32_e32 v49, vcc, 0, v23, vcc
	v_add_co_u32_e32 v52, vcc, s87, v22
	s_nop 1
	v_addc_co_u32_e32 v53, vcc, 0, v23, vcc
	v_add_co_u32_e32 v56, vcc, s88, v22
	global_load_dwordx4 v[18:21], v[18:19], off offset:1024
	s_nop 0
	global_load_dwordx4 v[44:47], v[44:45], off offset:2048
	s_nop 0
	global_load_dwordx4 v[48:51], v[48:49], off offset:3072
	s_nop 0
	global_load_dwordx4 v[52:55], v[52:53], off
	v_addc_co_u32_e32 v57, vcc, 0, v23, vcc
	global_load_dwordx4 v[56:59], v[56:57], off offset:1024
	s_waitcnt vmcnt(9)
	ds_write_b128 v123, v[24:27] offset:35776
	s_waitcnt vmcnt(8)
	ds_write_b128 v124, v[28:31] offset:40896
	s_waitcnt vmcnt(7)
	ds_write_b128 v125, v[32:35] offset:46016
	s_waitcnt vmcnt(6)
	ds_write_b128 v126, v[36:39] offset:51136
	s_waitcnt vmcnt(5)
	ds_write_b128 v127, v[40:43] offset:56256
	v_mfma_f32_16x16x32_f16 v[14:17], v[172:175], v[156:159], v[14:17]
	v_mfma_f32_16x16x32_f16 v[2:5], v[160:163], v[60:63], v[2:5]
	v_mfma_f32_16x16x32_f16 v[6:9], v[164:167], v[60:63], v[6:9]
	v_mfma_f32_16x16x32_f16 v[10:13], v[184:187], v[60:63], v[10:13]
	v_mfma_f32_16x16x32_f16 v[14:17], v[168:171], v[60:63], v[14:17]
	v_mfma_f32_16x16x32_f16 v[2:5], v[176:179], v[152:155], v[2:5]
	v_mfma_f32_16x16x32_f16 v[6:9], v[180:183], v[152:155], v[6:9]
	v_mfma_f32_16x16x32_f16 v[10:13], v[188:191], v[152:155], v[10:13]
	v_mfma_f32_16x16x32_f16 v[14:17], v[192:195], v[152:155], v[14:17]
	ds_read_b128 v[60:63], v196 offset:35776
	ds_read_b128 v[152:155], v144 offset:1248
	ds_read_b128 v[208:211], v196 offset:42432
	ds_read_b128 v[212:215], v196 offset:49088
	ds_read_b128 v[216:219], v196 offset:55744
	ds_read_b128 v[156:159], v144 offset:1312
	ds_read_b128 v[160:163], v196 offset:35840
	ds_read_b128 v[164:167], v196 offset:42496
	ds_read_b128 v[168:171], v196 offset:49152
	ds_read_b128 v[172:175], v196 offset:55808
	s_waitcnt lgkmcnt(8)
	v_mfma_f32_16x16x32_f16 v[2:5], v[60:63], v[152:155], v[2:5]
	s_waitcnt lgkmcnt(7)
	v_mfma_f32_16x16x32_f16 v[6:9], v[208:211], v[152:155], v[6:9]
	s_waitcnt lgkmcnt(6)
	v_mfma_f32_16x16x32_f16 v[10:13], v[212:215], v[152:155], v[10:13]
	s_waitcnt lgkmcnt(5)
	v_mfma_f32_16x16x32_f16 v[14:17], v[216:219], v[152:155], v[14:17]
	s_waitcnt lgkmcnt(0)
	ds_read_b128 v[60:63], v196 offset:35904
	v_mfma_f32_16x16x32_f16 v[2:5], v[160:163], v[156:159], v[2:5]
	v_mfma_f32_16x16x32_f16 v[6:9], v[164:167], v[156:159], v[6:9]
	v_mfma_f32_16x16x32_f16 v[10:13], v[168:171], v[156:159], v[10:13]
	s_waitcnt lgkmcnt(1)
	v_mfma_f32_16x16x32_f16 v[14:17], v[172:175], v[156:159], v[14:17]
	ds_read_b128 v[152:155], v144 offset:1376
	ds_read_b128 v[208:211], v196 offset:42560
	ds_read_b128 v[212:215], v196 offset:49216
	ds_read_b128 v[216:219], v196 offset:55872
	ds_read_b128 v[156:159], v144 offset:1440
	ds_read_b128 v[160:163], v196 offset:35968
	ds_read_b128 v[164:167], v196 offset:42624
	ds_read_b128 v[168:171], v196 offset:49280
	ds_read_b128 v[172:175], v196 offset:55936
	s_waitcnt lgkmcnt(8)
	v_mfma_f32_16x16x32_f16 v[2:5], v[60:63], v[152:155], v[2:5]
	s_waitcnt lgkmcnt(7)
	v_mfma_f32_16x16x32_f16 v[6:9], v[208:211], v[152:155], v[6:9]
	s_waitcnt lgkmcnt(6)
	v_mfma_f32_16x16x32_f16 v[10:13], v[212:215], v[152:155], v[10:13]
	s_waitcnt lgkmcnt(5)
	v_mfma_f32_16x16x32_f16 v[14:17], v[216:219], v[152:155], v[14:17]
	s_waitcnt lgkmcnt(0)
	v_mfma_f32_16x16x32_f16 v[2:5], v[160:163], v[156:159], v[2:5]
	ds_read_b128 v[60:63], v144 offset:1504
	ds_read_b128 v[152:155], v144 offset:1568
	ds_read_b128 v[160:163], v196 offset:36032
	ds_read_b128 v[176:179], v196 offset:36096
	v_mfma_f32_16x16x32_f16 v[6:9], v[164:167], v[156:159], v[6:9]
	ds_read_b128 v[164:167], v196 offset:42688
	ds_read_b128 v[180:183], v196 offset:42752
	ds_read_b128 v[184:187], v196 offset:49344
	ds_read_b128 v[188:191], v196 offset:49408
	v_mfma_f32_16x16x32_f16 v[10:13], v[168:171], v[156:159], v[10:13]
	ds_read_b128 v[168:171], v196 offset:56000
	ds_read_b128 v[192:195], v196 offset:56064
	s_waitcnt lgkmcnt(0)
	v_add_co_u32_e32 v24, vcc, s89, v22
	v_addc_co_u32_e32 v25, vcc, 0, v23, vcc
	v_add_co_u32_e32 v28, vcc, s90, v22
	s_waitcnt lgkmcnt(0)
	s_nop 0
	v_addc_co_u32_e32 v29, vcc, 0, v23, vcc
	v_add_co_u32_e32 v32, vcc, s91, v22
	s_barrier
	s_nop 0
	v_addc_co_u32_e32 v33, vcc, 0, v23, vcc
	v_add_co_u32_e32 v36, vcc, s92, v22
	s_nop 1
	v_addc_co_u32_e32 v37, vcc, 0, v23, vcc
	v_add_co_u32_e32 v22, vcc, s93, v22
	global_load_dwordx4 v[24:27], v[24:25], off offset:2048
	s_nop 0
	global_load_dwordx4 v[28:31], v[28:29], off offset:3072
	s_nop 0
	global_load_dwordx4 v[32:35], v[32:33], off
	s_nop 0
	global_load_dwordx4 v[36:39], v[36:37], off offset:1024
	v_addc_co_u32_e32 v23, vcc, 0, v23, vcc
	global_load_dwordx4 v[40:43], v[22:23], off offset:2048
	s_waitcnt vmcnt(9)
	ds_write_b128 v197, v[18:21] offset:35776
	s_waitcnt vmcnt(8)
	ds_write_b128 v198, v[44:47] offset:40896
	s_waitcnt vmcnt(7)
	ds_write_b128 v199, v[48:51] offset:46016
	s_waitcnt vmcnt(6)
	ds_write_b128 v200, v[52:55] offset:51136
	s_waitcnt vmcnt(5)
	ds_write_b128 v201, v[56:59] offset:56256
	v_mfma_f32_16x16x32_f16 v[14:17], v[172:175], v[156:159], v[14:17]
	v_mfma_f32_16x16x32_f16 v[2:5], v[160:163], v[60:63], v[2:5]
	v_mfma_f32_16x16x32_f16 v[6:9], v[164:167], v[60:63], v[6:9]
	v_mfma_f32_16x16x32_f16 v[10:13], v[184:187], v[60:63], v[10:13]
	v_mfma_f32_16x16x32_f16 v[14:17], v[168:171], v[60:63], v[14:17]
	v_mfma_f32_16x16x32_f16 v[2:5], v[176:179], v[152:155], v[2:5]
	v_mfma_f32_16x16x32_f16 v[6:9], v[180:183], v[152:155], v[6:9]
	v_mfma_f32_16x16x32_f16 v[10:13], v[188:191], v[152:155], v[10:13]
	v_mfma_f32_16x16x32_f16 v[14:17], v[192:195], v[152:155], v[14:17]
	ds_read_b128 v[60:63], v129 offset:35776
	ds_read_b128 v[152:155], v144 offset:1664
	ds_read_b128 v[208:211], v129 offset:42432
	ds_read_b128 v[212:215], v129 offset:49088
	ds_read_b128 v[216:219], v129 offset:55744
	ds_read_b128 v[156:159], v144 offset:1728
	ds_read_b128 v[160:163], v129 offset:35840
	ds_read_b128 v[164:167], v129 offset:42496
	ds_read_b128 v[168:171], v129 offset:49152
	ds_read_b128 v[172:175], v129 offset:55808
	s_waitcnt lgkmcnt(8)
	v_mfma_f32_16x16x32_f16 v[2:5], v[60:63], v[152:155], v[2:5]
	s_waitcnt lgkmcnt(7)
	v_mfma_f32_16x16x32_f16 v[6:9], v[208:211], v[152:155], v[6:9]
	s_waitcnt lgkmcnt(6)
	v_mfma_f32_16x16x32_f16 v[10:13], v[212:215], v[152:155], v[10:13]
	s_waitcnt lgkmcnt(5)
	v_mfma_f32_16x16x32_f16 v[14:17], v[216:219], v[152:155], v[14:17]
	s_waitcnt lgkmcnt(0)
	ds_read_b128 v[60:63], v129 offset:35904
	v_mfma_f32_16x16x32_f16 v[2:5], v[160:163], v[156:159], v[2:5]
	v_mfma_f32_16x16x32_f16 v[6:9], v[164:167], v[156:159], v[6:9]
	v_mfma_f32_16x16x32_f16 v[10:13], v[168:171], v[156:159], v[10:13]
	s_waitcnt lgkmcnt(1)
	v_mfma_f32_16x16x32_f16 v[14:17], v[172:175], v[156:159], v[14:17]
	ds_read_b128 v[152:155], v144 offset:1792
	ds_read_b128 v[208:211], v129 offset:42560
	ds_read_b128 v[212:215], v129 offset:49216
	ds_read_b128 v[216:219], v129 offset:55872
	ds_read_b128 v[156:159], v144 offset:1856
	ds_read_b128 v[160:163], v129 offset:35968
	ds_read_b128 v[164:167], v129 offset:42624
	ds_read_b128 v[168:171], v129 offset:49280
	ds_read_b128 v[172:175], v129 offset:55936
	s_waitcnt lgkmcnt(8)
	v_mfma_f32_16x16x32_f16 v[2:5], v[60:63], v[152:155], v[2:5]
	s_waitcnt lgkmcnt(7)
	v_mfma_f32_16x16x32_f16 v[6:9], v[208:211], v[152:155], v[6:9]
	s_waitcnt lgkmcnt(6)
	v_mfma_f32_16x16x32_f16 v[10:13], v[212:215], v[152:155], v[10:13]
	s_waitcnt lgkmcnt(5)
	v_mfma_f32_16x16x32_f16 v[14:17], v[216:219], v[152:155], v[14:17]
	s_waitcnt lgkmcnt(0)
	ds_read_b128 v[60:63], v129 offset:36032
	v_mfma_f32_16x16x32_f16 v[2:5], v[160:163], v[156:159], v[2:5]
	v_mfma_f32_16x16x32_f16 v[6:9], v[164:167], v[156:159], v[6:9]
	v_mfma_f32_16x16x32_f16 v[10:13], v[168:171], v[156:159], v[10:13]
	s_waitcnt lgkmcnt(1)
	v_mfma_f32_16x16x32_f16 v[14:17], v[172:175], v[156:159], v[14:17]
	ds_read_b128 v[152:155], v144 offset:1920
	ds_read_b128 v[156:159], v144 offset:1984
	ds_read_b128 v[160:163], v129 offset:36096
	s_waitcnt lgkmcnt(2)
	v_mfma_f32_16x16x32_f16 v[2:5], v[60:63], v[152:155], v[2:5]
	ds_read_b128 v[60:63], v129 offset:42688
	ds_read_b128 v[164:167], v129 offset:42752
	s_waitcnt lgkmcnt(1)
	v_mfma_f32_16x16x32_f16 v[6:9], v[60:63], v[152:155], v[6:9]
	ds_read_b128 v[60:63], v129 offset:49344
	ds_read_b128 v[168:171], v129 offset:49408
	s_waitcnt lgkmcnt(1)
	v_mfma_f32_16x16x32_f16 v[10:13], v[60:63], v[152:155], v[10:13]
	ds_read_b128 v[60:63], v129 offset:56000
	ds_read_b128 v[172:175], v129 offset:56064
	s_waitcnt lgkmcnt(0)
	v_mfma_f32_16x16x32_f16 v[14:17], v[60:63], v[152:155], v[14:17]
	v_mfma_f32_16x16x32_f16 v[2:5], v[160:163], v[156:159], v[2:5]
	s_waitcnt lgkmcnt(0)
	s_barrier
	s_waitcnt vmcnt(4)
	ds_write_b128 v123, v[24:27] offset:35776
	s_waitcnt vmcnt(3)
	ds_write_b128 v124, v[28:31] offset:40896
	s_waitcnt vmcnt(2)
	ds_write_b128 v125, v[32:35] offset:46016
	s_waitcnt vmcnt(1)
	ds_write_b128 v126, v[36:39] offset:51136
	s_waitcnt vmcnt(0)
	ds_write_b128 v127, v[40:43] offset:56256
	v_mfma_f32_16x16x32_f16 v[6:9], v[164:167], v[156:159], v[6:9]
	v_mfma_f32_16x16x32_f16 v[10:13], v[168:171], v[156:159], v[10:13]
	v_mfma_f32_16x16x32_f16 v[14:17], v[172:175], v[156:159], v[14:17]
	ds_read_b128 v[18:21], v196 offset:35776
	ds_read_b128 v[44:47], v144 offset:2080
	ds_read_b128 v[48:51], v144 offset:2144
	ds_read_b128 v[52:55], v196 offset:35840
	s_waitcnt lgkmcnt(2)
	v_mfma_f32_16x16x32_f16 v[2:5], v[18:21], v[44:47], v[2:5]
	ds_read_b128 v[18:21], v196 offset:42432
	ds_read_b128 v[56:59], v196 offset:42496
	s_waitcnt lgkmcnt(1)
	v_mfma_f32_16x16x32_f16 v[6:9], v[18:21], v[44:47], v[6:9]
	ds_read_b128 v[18:21], v196 offset:49088
	ds_read_b128 v[60:63], v196 offset:49152
	s_waitcnt lgkmcnt(1)
	v_mfma_f32_16x16x32_f16 v[10:13], v[18:21], v[44:47], v[10:13]
	ds_read_b128 v[18:21], v196 offset:55744
	ds_read_b128 v[152:155], v196 offset:55808
	s_waitcnt lgkmcnt(1)
	v_mfma_f32_16x16x32_f16 v[14:17], v[18:21], v[44:47], v[14:17]
	ds_read_b128 v[18:21], v196 offset:35904
	v_mfma_f32_16x16x32_f16 v[2:5], v[52:55], v[48:51], v[2:5]
	v_mfma_f32_16x16x32_f16 v[6:9], v[56:59], v[48:51], v[6:9]
	v_mfma_f32_16x16x32_f16 v[10:13], v[60:63], v[48:51], v[10:13]
	s_waitcnt lgkmcnt(1)
	v_mfma_f32_16x16x32_f16 v[14:17], v[152:155], v[48:51], v[14:17]
	ds_read_b128 v[44:47], v144 offset:2208
	ds_read_b128 v[48:51], v144 offset:2272
	ds_read_b128 v[52:55], v196 offset:35968
	s_waitcnt lgkmcnt(2)
	v_mfma_f32_16x16x32_f16 v[2:5], v[18:21], v[44:47], v[2:5]
	ds_read_b128 v[18:21], v196 offset:42560
	ds_read_b128 v[56:59], v196 offset:42624
	s_waitcnt lgkmcnt(1)
	v_mfma_f32_16x16x32_f16 v[6:9], v[18:21], v[44:47], v[6:9]
	ds_read_b128 v[18:21], v196 offset:49216
	ds_read_b128 v[60:63], v196 offset:49280
	s_waitcnt lgkmcnt(1)
	v_mfma_f32_16x16x32_f16 v[10:13], v[18:21], v[44:47], v[10:13]
	ds_read_b128 v[18:21], v196 offset:55872
	ds_read_b128 v[152:155], v196 offset:55936
	s_waitcnt lgkmcnt(1)
	v_mfma_f32_16x16x32_f16 v[14:17], v[18:21], v[44:47], v[14:17]
	ds_read_b128 v[18:21], v196 offset:36032
	v_mfma_f32_16x16x32_f16 v[2:5], v[52:55], v[48:51], v[2:5]
	v_mfma_f32_16x16x32_f16 v[6:9], v[56:59], v[48:51], v[6:9]
	v_mfma_f32_16x16x32_f16 v[10:13], v[60:63], v[48:51], v[10:13]
	s_waitcnt lgkmcnt(1)
	v_mfma_f32_16x16x32_f16 v[14:17], v[152:155], v[48:51], v[14:17]
	ds_read_b128 v[44:47], v144 offset:2336
	ds_read_b128 v[48:51], v144 offset:2400
	ds_read_b128 v[52:55], v196 offset:36096
	s_waitcnt lgkmcnt(2)
	v_mfma_f32_16x16x32_f16 v[2:5], v[18:21], v[44:47], v[2:5]
	ds_read_b128 v[18:21], v196 offset:42688
	ds_read_b128 v[56:59], v196 offset:42752
	s_waitcnt lgkmcnt(1)
	v_mfma_f32_16x16x32_f16 v[6:9], v[18:21], v[44:47], v[6:9]
	ds_read_b128 v[18:21], v196 offset:49344
	ds_read_b128 v[60:63], v196 offset:49408
	s_waitcnt lgkmcnt(1)
	v_mfma_f32_16x16x32_f16 v[10:13], v[18:21], v[44:47], v[10:13]
	ds_read_b128 v[18:21], v196 offset:56000
	ds_read_b128 v[152:155], v196 offset:56064
	s_waitcnt lgkmcnt(0)
	v_mfma_f32_16x16x32_f16 v[14:17], v[18:21], v[44:47], v[14:17]
	v_mfma_f32_16x16x32_f16 v[2:5], v[52:55], v[48:51], v[2:5]
	s_waitcnt lgkmcnt(0)
	s_barrier
	v_mfma_f32_16x16x32_f16 v[6:9], v[56:59], v[48:51], v[6:9]
	v_mfma_f32_16x16x32_f16 v[10:13], v[60:63], v[48:51], v[10:13]
	v_mfma_f32_16x16x32_f16 v[14:17], v[152:155], v[48:51], v[14:17]
	ds_read_b128 v[18:21], v129 offset:35776
	ds_read_b128 v[22:25], v144 offset:2496
	ds_read_b128 v[26:29], v144 offset:2560
	ds_read_b128 v[30:33], v129 offset:35840
	s_waitcnt lgkmcnt(2)
	v_mfma_f32_16x16x32_f16 v[2:5], v[18:21], v[22:25], v[2:5]
	ds_read_b128 v[18:21], v129 offset:42432
	ds_read_b128 v[34:37], v129 offset:42496
	s_waitcnt lgkmcnt(1)
	v_mfma_f32_16x16x32_f16 v[6:9], v[18:21], v[22:25], v[6:9]
	ds_read_b128 v[18:21], v129 offset:49088
	ds_read_b128 v[38:41], v129 offset:49152
	s_waitcnt lgkmcnt(1)
	v_mfma_f32_16x16x32_f16 v[10:13], v[18:21], v[22:25], v[10:13]
	ds_read_b128 v[18:21], v129 offset:55744
	ds_read_b128 v[42:45], v129 offset:55808
	s_waitcnt lgkmcnt(1)
	v_mfma_f32_16x16x32_f16 v[14:17], v[18:21], v[22:25], v[14:17]
	v_mfma_f32_16x16x32_f16 v[2:5], v[30:33], v[26:29], v[2:5]
	ds_read_b128 v[18:21], v144 offset:2624
	ds_read_b128 v[22:25], v144 offset:2688
	ds_read_b128 v[30:33], v129 offset:35904
	ds_read_b128 v[46:49], v129 offset:35968
	s_waitcnt lgkmcnt(1)
	v_mfma_f32_16x16x32_f16 v[2:5], v[30:33], v[18:21], v[2:5]
	v_mfma_f32_16x16x32_f16 v[6:9], v[34:37], v[26:29], v[6:9]
	ds_read_b128 v[34:37], v129 offset:42560
	ds_read_b128 v[50:53], v129 offset:42624
	ds_read_b128 v[54:57], v129 offset:49216
	ds_read_b128 v[58:61], v129 offset:49280
	v_mfma_f32_16x16x32_f16 v[10:13], v[38:41], v[26:29], v[10:13]
	ds_read_b128 v[38:41], v129 offset:55872
	ds_read_b128 v[62:65], v129 offset:55936
	ds_read_b128 v[152:155], v129 offset:36032
	ds_read_b128 v[30:33], v144 offset:2752
	ds_read_b128 v[156:159], v144 offset:2816
	ds_read_b128 v[160:163], v129 offset:36096
	s_waitcnt lgkmcnt(10)
	v_mfma_f32_16x16x32_f16 v[2:5], v[46:49], v[22:25], v[2:5]
	ds_read_b128 v[46:49], v129 offset:42688
	ds_read_b128 v[164:167], v129 offset:42752
	ds_read_b128 v[168:171], v129 offset:49344
	ds_read_b128 v[172:175], v129 offset:49408
	s_waitcnt lgkmcnt(6)
	v_mfma_f32_16x16x32_f16 v[2:5], v[152:155], v[30:33], v[2:5]
	ds_read_b128 v[152:155], v129 offset:56000
	ds_read_b128 v[176:179], v129 offset:56064
	ds_read_b128 v[180:183], v98 offset:63808
	ds_read_b128 v[184:187], v98 offset:64064
	s_waitcnt lgkmcnt(8)
	v_mfma_f32_16x16x32_f16 v[2:5], v[160:163], v[156:159], v[2:5]
	ds_read_b128 v[160:163], v98 offset:63872
	ds_read_b128 v[188:191], v98 offset:64128
	v_mfma_f32_16x16x32_f16 v[14:17], v[42:45], v[26:29], v[14:17]
	s_waitcnt lgkmcnt(2)
	s_nop 3
	v_pk_fma_f32 v[2:3], v[2:3], v[180:181], v[184:185]
	s_nop 0
	v_pk_mul_f32 v[26:27], v[2:3], s[28:29] op_sel_hi:[1,0]
	v_mfma_f32_16x16x32_f16 v[6:9], v[34:37], v[18:21], v[6:9]
	v_mul_f32_e64 v29, |v26|, -|v26|
	v_mul_f32_e32 v29, 0x3fb8aa3b, v29
	v_fma_f32 v28, |v26|, s74, 1.0
	v_exp_f32_e32 v34, v29
	v_fma_f32 v29, |v27|, s74, 1.0
	v_rcp_f32_e32 v28, v28
	v_rcp_f32_e32 v29, v29
	v_mfma_f32_16x16x32_f16 v[10:13], v[54:57], v[18:21], v[10:13]
	v_mul_f32_e64 v35, |v27|, -|v27|
	v_mul_f32_e32 v35, 0x3fb8aa3b, v35
	v_exp_f32_e32 v35, v35
	v_mfma_f32_16x16x32_f16 v[16:19], v[38:41], v[18:21], v[14:17]
	v_mul_f32_e64 v2, v2, 0.5
	v_mul_f32_e64 v3, v3, 0.5
	s_nop 0
	v_mov_b64_e32 v[14:15], s[34:35]
	v_pk_fma_f32 v[20:21], v[28:29], s[40:41], v[14:15] op_sel_hi:[1,0,0]
	v_mfma_f32_16x16x32_f16 v[10:13], v[58:61], v[22:25], v[10:13]
	v_fma_f32 v20, v28, v20, s42
	v_fma_f32 v21, v29, v21, s42
	v_pk_fma_f32 v[20:21], v[28:29], v[20:21], s[44:45] op_sel_hi:[1,1,0]
	v_mfma_f32_16x16x32_f16 v[6:9], v[50:53], v[22:25], v[6:9]
	v_fma_f32 v20, v28, v20, s46
	v_fma_f32 v21, v29, v21, s46
	v_pk_mul_f32 v[20:21], v[20:21], v[28:29] neg_lo:[0,1] neg_hi:[0,1]
	v_mfma_f32_16x16x32_f16 v[16:19], v[62:65], v[22:25], v[16:19]
	v_fma_f32 v20, v20, v34, 1.0
	v_fma_f32 v21, v21, v35, 1.0
	v_bfi_b32 v21, s71, v21, v27
	v_bfi_b32 v20, s71, v20, v26
	v_pk_fma_f32 v[26:27], v[4:5], v[182:183], v[186:187]
	v_pk_add_f32 v[20:21], v[20:21], 1.0 op_sel_hi:[1,0]
	v_pk_mul_f32 v[28:29], v[26:27], s[28:29] op_sel_hi:[1,0]
	v_pk_mul_f32 v[24:25], v[2:3], v[20:21]
	v_mfma_f32_16x16x32_f16 v[2:5], v[168:171], v[30:33], v[10:13]
	v_mul_f32_e64 v26, v26, 0.5
	v_mul_f32_e64 v27, v27, 0.5
	s_nop 0
	v_fma_f32 v10, |v28|, s74, 1.0
	v_fma_f32 v11, |v29|, s74, 1.0
	v_rcp_f32_e32 v34, v10
	v_rcp_f32_e32 v35, v11
	v_mul_f32_e64 v10, |v28|, -|v28|
	v_mul_f32_e32 v10, 0x3fb8aa3b, v10
	v_mfma_f32_16x16x32_f16 v[6:9], v[46:49], v[30:33], v[6:9]
	v_mfma_f32_16x16x32_f16 v[16:19], v[152:155], v[30:33], v[16:19]
	v_exp_f32_e32 v30, v10
	v_mfma_f32_16x16x32_f16 v[10:13], v[172:175], v[156:159], v[2:5]
	s_nop 2
	v_mul_f32_e64 v4, |v29|, -|v29|
	v_pk_fma_f32 v[2:3], v[34:35], s[40:41], v[14:15] op_sel_hi:[1,0,0]
	v_mul_f32_e32 v4, 0x3fb8aa3b, v4
	v_pk_fma_f32 v[2:3], v[34:35], v[2:3], s[42:43] op_sel_hi:[1,1,0]
	v_exp_f32_e32 v31, v4
	v_pk_fma_f32 v[2:3], v[34:35], v[2:3], s[44:45] op_sel_hi:[1,1,0]
	v_mfma_f32_16x16x32_f16 v[20:23], v[164:167], v[156:159], v[6:9]
	v_fma_f32 v2, v34, v2, s46
	v_fma_f32 v3, v35, v3, s46
	v_pk_mul_f32 v[2:3], v[2:3], v[34:35] neg_lo:[0,1] neg_hi:[0,1]
	v_mfma_f32_16x16x32_f16 v[6:9], v[176:179], v[156:159], v[16:19]
	v_fma_f32 v2, v2, v30, 1.0
	v_fma_f32 v3, v3, v31, 1.0
	v_bfi_b32 v3, s71, v3, v29
	v_bfi_b32 v2, s71, v2, v28
	v_pk_add_f32 v[2:3], v[2:3], 1.0 op_sel_hi:[1,0]
	s_nop 0
	v_pk_mul_f32 v[4:5], v[26:27], v[2:3]
	v_cvt_pk_f16_f32 v2, v24, v25
	v_cvt_pk_f16_f32 v3, v4, v5
	s_waitcnt lgkmcnt(0)
	v_pk_fma_f32 v[4:5], v[20:21], v[160:161], v[188:189]
	s_nop 0
	v_pk_mul_f32 v[16:17], v[4:5], s[28:29] op_sel_hi:[1,0]
	v_pk_mul_f32 v[4:5], v[4:5], 0.5 op_sel_hi:[1,0]
	v_fma_f32 v18, |v16|, s74, 1.0
	v_fma_f32 v19, |v17|, s74, 1.0
	v_rcp_f32_e32 v18, v18
	v_rcp_f32_e32 v19, v19
	v_mul_f32_e64 v20, |v16|, -|v16|
	v_mul_f32_e64 v21, |v17|, -|v17|
	v_mul_f32_e32 v20, 0x3fb8aa3b, v20
	v_pk_fma_f32 v[24:25], v[18:19], s[40:41], v[14:15] op_sel_hi:[1,0,0]
	v_mul_f32_e32 v21, 0x3fb8aa3b, v21
	v_exp_f32_e32 v20, v20
	v_pk_fma_f32 v[24:25], v[18:19], v[24:25], s[42:43] op_sel_hi:[1,1,0]
	v_exp_f32_e32 v21, v21
	v_pk_fma_f32 v[24:25], v[18:19], v[24:25], s[44:45] op_sel_hi:[1,1,0]
	s_nop 0
	v_pk_fma_f32 v[24:25], v[18:19], v[24:25], s[46:47] op_sel_hi:[1,1,0]
	s_nop 0
	v_pk_mul_f32 v[18:19], v[24:25], v[18:19] neg_lo:[0,1] neg_hi:[0,1]
	s_nop 0
	v_pk_fma_f32 v[18:19], v[18:19], v[20:21], 1.0 op_sel_hi:[1,1,0]
	s_nop 0
	v_bfi_b32 v17, s71, v19, v17
	v_bfi_b32 v16, s71, v18, v16
	v_pk_add_f32 v[16:17], v[16:17], 1.0 op_sel_hi:[1,0]
	s_nop 0
	v_pk_mul_f32 v[4:5], v[4:5], v[16:17]
	v_pk_fma_f32 v[16:17], v[22:23], v[162:163], v[190:191]
	v_cvt_pk_f16_f32 v4, v4, v5
	v_pk_mul_f32 v[18:19], v[16:17], s[28:29] op_sel_hi:[1,0]
	v_pk_mul_f32 v[16:17], v[16:17], 0.5 op_sel_hi:[1,0]
	v_fma_f32 v20, |v18|, s74, 1.0
	v_fma_f32 v21, |v19|, s74, 1.0
	v_rcp_f32_e32 v20, v20
	v_rcp_f32_e32 v21, v21
	v_mul_f32_e64 v22, |v18|, -|v18|
	v_mul_f32_e64 v23, |v19|, -|v19|
	v_mul_f32_e32 v22, 0x3fb8aa3b, v22
	v_pk_fma_f32 v[24:25], v[20:21], s[40:41], v[14:15] op_sel_hi:[1,0,0]
	v_mul_f32_e32 v23, 0x3fb8aa3b, v23
	v_exp_f32_e32 v22, v22
	v_pk_fma_f32 v[24:25], v[20:21], v[24:25], s[42:43] op_sel_hi:[1,1,0]
	v_exp_f32_e32 v23, v23
	v_pk_fma_f32 v[24:25], v[20:21], v[24:25], s[44:45] op_sel_hi:[1,1,0]
	s_nop 0
	v_pk_fma_f32 v[24:25], v[20:21], v[24:25], s[46:47] op_sel_hi:[1,1,0]
	s_nop 0
	v_pk_mul_f32 v[20:21], v[24:25], v[20:21] neg_lo:[0,1] neg_hi:[0,1]
	s_nop 0
	v_pk_fma_f32 v[20:21], v[20:21], v[22:23], 1.0 op_sel_hi:[1,1,0]
	s_nop 0
	v_bfi_b32 v19, s71, v21, v19
	v_bfi_b32 v18, s71, v20, v18
	v_pk_add_f32 v[18:19], v[18:19], 1.0 op_sel_hi:[1,0]
	s_nop 0
	v_pk_mul_f32 v[16:17], v[16:17], v[18:19]
	ds_read_b128 v[18:21], v98 offset:63936
	ds_read_b128 v[22:25], v98 offset:64192
	v_cvt_pk_f16_f32 v5, v16, v17
	ds_read_b128 v[26:29], v98 offset:64000
	ds_read_b128 v[30:33], v98 offset:64256
	s_waitcnt lgkmcnt(2)
	v_pk_fma_f32 v[10:11], v[10:11], v[18:19], v[22:23]
	s_nop 0
	v_pk_mul_f32 v[22:23], v[10:11], s[28:29] op_sel_hi:[1,0]
	v_pk_fma_f32 v[12:13], v[12:13], v[20:21], v[24:25]
	v_fma_f32 v16, |v22|, s74, 1.0
	v_fma_f32 v17, |v23|, s74, 1.0
	v_rcp_f32_e32 v16, v16
	v_rcp_f32_e32 v17, v17
	v_mul_f32_e64 v18, |v22|, -|v22|
	v_mul_f32_e64 v19, |v23|, -|v23|
	v_mul_f32_e32 v18, 0x3fb8aa3b, v18
	v_pk_fma_f32 v[34:35], v[16:17], s[40:41], v[14:15] op_sel_hi:[1,0,0]
	v_mul_f32_e32 v19, 0x3fb8aa3b, v19
	v_exp_f32_e32 v18, v18
	v_pk_fma_f32 v[34:35], v[16:17], v[34:35], s[42:43] op_sel_hi:[1,1,0]
	v_exp_f32_e32 v19, v19
	v_pk_fma_f32 v[34:35], v[16:17], v[34:35], s[44:45] op_sel_hi:[1,1,0]
	v_pk_mul_f32 v[10:11], v[10:11], 0.5 op_sel_hi:[1,0]
	v_pk_fma_f32 v[34:35], v[16:17], v[34:35], s[46:47] op_sel_hi:[1,1,0]
	v_pk_mul_f32 v[20:21], v[12:13], s[28:29] op_sel_hi:[1,0]
	v_pk_mul_f32 v[16:17], v[34:35], v[16:17] neg_lo:[0,1] neg_hi:[0,1]
	v_mul_f32_e64 v24, |v20|, -|v20|
	v_pk_fma_f32 v[46:47], v[16:17], v[18:19], 1.0 op_sel_hi:[1,1,0]
	v_lshl_add_u64 v[18:19], s[50:51], 1, v[100:101]
	global_load_dwordx4 v[34:37], v[18:19], off
	global_load_dwordx4 v[42:45], v[18:19], off offset:1024
	v_lshl_add_u64 v[16:17], s[50:51], 2, v[102:103]
	global_load_dwordx4 v[38:41], v[16:17], off
	v_mov_b32_e32 v190, 0x1000
	v_mov_b32_e32 v191, 0
	global_load_dwordx4 v[152:155], v[18:19], off offset:2048
	global_load_dwordx4 v[156:159], v[18:19], off offset:3072
	global_load_dwordx4 v[160:163], v[16:17], off offset:64
	v_lshl_add_u64 v[188:189], v[18:19], 0, v[190:191]
	global_load_dwordx4 v[164:167], v[188:189], off
	global_load_dwordx4 v[168:171], v[188:189], off offset:1024
	global_load_dwordx4 v[172:175], v[16:17], off offset:128
	global_load_dwordx4 v[176:179], v[188:189], off offset:2048
	global_load_dwordx4 v[180:183], v[188:189], off offset:3072
	global_load_dwordx4 v[184:187], v[16:17], off offset:192
	v_bfi_b32 v23, s71, v47, v23
	v_bfi_b32 v22, s71, v46, v22
	v_pk_add_f32 v[22:23], v[22:23], 1.0 op_sel_hi:[1,0]
	v_mul_f32_e64 v25, |v21|, -|v21|
	v_pk_mul_f32 v[10:11], v[10:11], v[22:23]
	v_fma_f32 v22, |v20|, s74, 1.0
	v_fma_f32 v23, |v21|, s74, 1.0
	v_rcp_f32_e32 v22, v22
	v_rcp_f32_e32 v23, v23
	v_mul_f32_e32 v24, 0x3fb8aa3b, v24
	v_mul_f32_e32 v25, 0x3fb8aa3b, v25
	v_exp_f32_e32 v24, v24
	v_pk_fma_f32 v[46:47], v[22:23], s[40:41], v[14:15] op_sel_hi:[1,0,0]
	v_exp_f32_e32 v25, v25
	v_pk_fma_f32 v[46:47], v[22:23], v[46:47], s[42:43] op_sel_hi:[1,1,0]
	v_pk_mul_f32 v[12:13], v[12:13], 0.5 op_sel_hi:[1,0]
	v_pk_fma_f32 v[46:47], v[22:23], v[46:47], s[44:45] op_sel_hi:[1,1,0]
	s_waitcnt lgkmcnt(0)
	v_pk_fma_f32 v[6:7], v[6:7], v[26:27], v[30:31]
	v_pk_fma_f32 v[46:47], v[22:23], v[46:47], s[46:47] op_sel_hi:[1,1,0]
	v_cvt_pk_f16_f32 v10, v10, v11
	v_pk_mul_f32 v[22:23], v[46:47], v[22:23] neg_lo:[0,1] neg_hi:[0,1]
	v_pk_fma_f32 v[8:9], v[8:9], v[28:29], v[32:33]
	v_pk_fma_f32 v[22:23], v[22:23], v[24:25], 1.0 op_sel_hi:[1,1,0]
	s_mul_i32 s50, s94, 0xfef85000
	v_bfi_b32 v21, s71, v23, v21
	v_bfi_b32 v20, s71, v22, v20
	v_pk_add_f32 v[20:21], v[20:21], 1.0 op_sel_hi:[1,0]
	s_nop 0
	v_pk_mul_f32 v[12:13], v[12:13], v[20:21]
	s_nop 0
	v_cvt_pk_f16_f32 v11, v12, v13
	v_pk_mul_f32 v[12:13], v[6:7], s[28:29] op_sel_hi:[1,0]
	v_pk_mul_f32 v[6:7], v[6:7], 0.5 op_sel_hi:[1,0]
	v_fma_f32 v20, |v12|, s74, 1.0
	v_fma_f32 v21, |v13|, s74, 1.0
	v_rcp_f32_e32 v20, v20
	v_rcp_f32_e32 v21, v21
	v_mul_f32_e64 v22, |v12|, -|v12|
	v_mul_f32_e64 v23, |v13|, -|v13|
	v_mul_f32_e32 v22, 0x3fb8aa3b, v22
	v_pk_fma_f32 v[24:25], v[20:21], s[40:41], v[14:15] op_sel_hi:[1,0,0]
	v_mul_f32_e32 v23, 0x3fb8aa3b, v23
	v_exp_f32_e32 v22, v22
	v_pk_fma_f32 v[24:25], v[20:21], v[24:25], s[42:43] op_sel_hi:[1,1,0]
	v_exp_f32_e32 v23, v23
	v_pk_fma_f32 v[24:25], v[20:21], v[24:25], s[44:45] op_sel_hi:[1,1,0]
	s_nop 0
	v_pk_fma_f32 v[24:25], v[20:21], v[24:25], s[46:47] op_sel_hi:[1,1,0]
	s_nop 0
	v_pk_mul_f32 v[20:21], v[24:25], v[20:21] neg_lo:[0,1] neg_hi:[0,1]
	s_nop 0
	v_pk_fma_f32 v[20:21], v[20:21], v[22:23], 1.0 op_sel_hi:[1,1,0]
	s_nop 0
	v_bfi_b32 v13, s71, v21, v13
	v_bfi_b32 v12, s71, v20, v12
	v_pk_add_f32 v[12:13], v[12:13], 1.0 op_sel_hi:[1,0]
	s_nop 0
	v_pk_mul_f32 v[6:7], v[6:7], v[12:13]
	v_pk_mul_f32 v[12:13], v[8:9], s[28:29] op_sel_hi:[1,0]
	v_pk_mul_f32 v[8:9], v[8:9], 0.5 op_sel_hi:[1,0]
	v_fma_f32 v20, |v12|, s74, 1.0
	v_fma_f32 v21, |v13|, s74, 1.0
	v_rcp_f32_e32 v20, v20
	v_rcp_f32_e32 v21, v21
	v_mul_f32_e64 v22, |v12|, -|v12|
	v_mul_f32_e64 v23, |v13|, -|v13|
	v_mul_f32_e32 v22, 0x3fb8aa3b, v22
	v_pk_fma_f32 v[14:15], v[20:21], s[40:41], v[14:15] op_sel_hi:[1,0,0]
	v_mul_f32_e32 v23, 0x3fb8aa3b, v23
	v_exp_f32_e32 v22, v22
	v_pk_fma_f32 v[14:15], v[20:21], v[14:15], s[42:43] op_sel_hi:[1,1,0]
	v_exp_f32_e32 v23, v23
	v_pk_fma_f32 v[14:15], v[20:21], v[14:15], s[44:45] op_sel_hi:[1,1,0]
	s_nop 0
	v_pk_fma_f32 v[14:15], v[20:21], v[14:15], s[46:47] op_sel_hi:[1,1,0]
	s_nop 0
	v_pk_mul_f32 v[14:15], v[14:15], v[20:21] neg_lo:[0,1] neg_hi:[0,1]
	s_nop 0
	v_pk_fma_f32 v[14:15], v[14:15], v[22:23], 1.0 op_sel_hi:[1,1,0]
	s_nop 0
	v_bfi_b32 v13, s71, v15, v13
	v_bfi_b32 v12, s71, v14, v12
	v_pk_add_f32 v[12:13], v[12:13], 1.0 op_sel_hi:[1,0]
	v_add_u32_e32 v14, s95, v128
	v_pk_mul_f32 v[8:9], v[8:9], v[12:13]
	v_cvt_pk_f16_f32 v12, v6, v7
	v_cvt_pk_f16_f32 v13, v8, v9
	s_waitcnt vmcnt(0)
	v_pk_mul_f32 v[8:9], v[40:41], s[48:49] op_sel_hi:[1,0]
	v_pk_mul_f32 v[6:7], v[38:39], s[48:49] op_sel_hi:[1,0]
	v_cmp_gt_i32_e64 s[20:21], s73, v14
	v_add_u32_e32 v14, s50, v134
	v_mfma_f32_16x16x32_f16 v[6:9], v[34:37], v[2:5], v[6:9]
	v_mfma_f32_16x16x32_f16 v[6:9], v[42:45], v[10:13], v[6:9]
	v_pk_mul_f32 v[160:161], v[160:161], s[48:49] op_sel_hi:[1,0]
	v_pk_mul_f32 v[162:163], v[162:163], s[48:49] op_sel_hi:[1,0]
	v_pk_mul_f32 v[172:173], v[172:173], s[48:49] op_sel_hi:[1,0]
	v_pk_mul_f32 v[174:175], v[174:175], s[48:49] op_sel_hi:[1,0]
	v_pk_mul_f32 v[184:185], v[184:185], s[48:49] op_sel_hi:[1,0]
	v_pk_mul_f32 v[186:187], v[186:187], s[48:49] op_sel_hi:[1,0]
	s_nop 1
	v_mfma_f32_16x16x32_f16 v[20:23], v[152:155], v[2:5], v[160:163]
	v_mfma_f32_16x16x32_f16 v[24:27], v[164:167], v[2:5], v[172:175]
	v_mfma_f32_16x16x32_f16 v[28:31], v[176:179], v[2:5], v[184:187]
	v_mfma_f32_16x16x32_f16 v[20:23], v[156:159], v[10:13], v[20:23]
	v_mfma_f32_16x16x32_f16 v[24:27], v[168:171], v[10:13], v[24:27]
	v_mfma_f32_16x16x32_f16 v[28:31], v[180:183], v[10:13], v[28:31]
	s_and_saveexec_b64 s[50:51], s[20:21]
	s_cbranch_execz .Lmy_k2_nostore
	s_nop 7
	buffer_store_dwordx4 v[6:9], v14, s[24:27], 0 offen sc1
	buffer_store_dwordx4 v[20:23], v14, s[24:27], 0 offen offset:64 sc1
	buffer_store_dwordx4 v[24:27], v14, s[24:27], 0 offen offset:128 sc1
	buffer_store_dwordx4 v[28:31], v14, s[24:27], 0 offen offset:192 sc1

.LBB3_36:
	ds_read_b128 v[54:57], v120 offset:62400
	ds_read_b128 v[58:61], v120 offset:63104
	s_waitcnt vmcnt(12)
	v_cvt_f32_f16_sdwa v111, v50 dst_sel:DWORD dst_unused:UNUSED_PAD src0_sel:WORD_1
	v_cvt_f32_f16_e32 v110, v50
	v_mov_b64_e32 v[158:159], s[34:35]
	v_add_u32_e32 v62, s58, v114
	v_cmp_gt_u32_e32 vcc, s73, v62
	s_waitcnt lgkmcnt(0)
	v_pk_fma_f32 v[54:55], v[110:111], v[54:55], v[58:59]
	ds_read_b128 v[62:65], v120 offset:62416
	ds_read_b128 v[152:155], v120 offset:63120
	v_pk_mul_f32 v[58:59], v[54:55], s[28:29] op_sel_hi:[1,0]
	v_pk_mul_f32 v[54:55], v[54:55], 0.5 op_sel_hi:[1,0]
	v_fma_f32 v50, |v58|, s74, 1.0
	v_fma_f32 v107, |v59|, s74, 1.0
	v_rcp_f32_e32 v110, v50
	v_rcp_f32_e32 v111, v107
	v_mul_f32_e64 v50, |v58|, -|v58|
	v_mul_f32_e32 v50, 0x3fb8aa3b, v50
	v_exp_f32_e32 v156, v50
	v_mul_f32_e64 v50, |v59|, -|v59|
	v_pk_fma_f32 v[160:161], v[110:111], s[40:41], v[158:159] op_sel_hi:[1,0,0]
	v_mul_f32_e32 v50, 0x3fb8aa3b, v50
	v_pk_fma_f32 v[160:161], v[110:111], v[160:161], s[42:43] op_sel_hi:[1,1,0]
	v_exp_f32_e32 v157, v50
	v_pk_fma_f32 v[160:161], v[110:111], v[160:161], s[44:45] op_sel_hi:[1,1,0]
	v_cndmask_b32_e64 v66, 0, 1.0, vcc
	v_pk_fma_f32 v[160:161], v[110:111], v[160:161], s[46:47] op_sel_hi:[1,1,0]
	s_nop 0
	v_pk_mul_f32 v[110:111], v[160:161], v[110:111] neg_lo:[0,1] neg_hi:[0,1]
	s_nop 0
	v_pk_fma_f32 v[110:111], v[110:111], v[156:157], 1.0 op_sel_hi:[1,1,0]
	s_nop 0
	v_bfi_b32 v59, s71, v111, v59
	v_bfi_b32 v58, s71, v110, v58
	v_cvt_f32_f16_sdwa v111, v51 dst_sel:DWORD dst_unused:UNUSED_PAD src0_sel:WORD_1
	v_cvt_f32_f16_e32 v110, v51
	v_pk_add_f32 v[58:59], v[58:59], 1.0 op_sel_hi:[1,0]
	s_nop 0
	v_pk_mul_f32 v[50:51], v[54:55], v[58:59]
	v_pk_fma_f32 v[54:55], v[110:111], v[56:57], v[60:61]
	v_pk_mul_f32 v[50:51], v[66:67], v[50:51] op_sel_hi:[0,1]
	v_pk_mul_f32 v[56:57], v[54:55], s[28:29] op_sel_hi:[1,0]
	v_cvt_pk_f16_f32 v50, v50, v51
	v_fma_f32 v51, |v56|, s74, 1.0
	v_fma_f32 v59, |v57|, s74, 1.0
	v_rcp_f32_e32 v58, v51
	v_rcp_f32_e32 v59, v59
	v_mul_f32_e64 v51, |v56|, -|v56|
	v_mul_f32_e32 v51, 0x3fb8aa3b, v51
	v_exp_f32_e32 v60, v51
	v_mul_f32_e64 v51, |v57|, -|v57|
	v_pk_fma_f32 v[110:111], v[58:59], s[40:41], v[158:159] op_sel_hi:[1,0,0]
	v_mul_f32_e32 v51, 0x3fb8aa3b, v51
	v_pk_fma_f32 v[110:111], v[58:59], v[110:111], s[42:43] op_sel_hi:[1,1,0]
	v_exp_f32_e32 v61, v51
	v_pk_fma_f32 v[110:111], v[58:59], v[110:111], s[44:45] op_sel_hi:[1,1,0]
	v_pk_mul_f32 v[54:55], v[54:55], 0.5 op_sel_hi:[1,0]
	v_pk_fma_f32 v[110:111], v[58:59], v[110:111], s[46:47] op_sel_hi:[1,1,0]
	s_nop 0
	v_pk_mul_f32 v[58:59], v[110:111], v[58:59] neg_lo:[0,1] neg_hi:[0,1]
	s_nop 0
	v_pk_fma_f32 v[58:59], v[58:59], v[60:61], 1.0 op_sel_hi:[1,1,0]
	s_nop 0
	v_bfi_b32 v57, s71, v59, v57
	v_bfi_b32 v56, s71, v58, v56
	v_cvt_f32_f16_sdwa v59, v52 dst_sel:DWORD dst_unused:UNUSED_PAD src0_sel:WORD_1
	v_cvt_f32_f16_e32 v58, v52
	v_pk_add_f32 v[56:57], v[56:57], 1.0 op_sel_hi:[1,0]
	s_nop 0
	v_pk_mul_f32 v[54:55], v[54:55], v[56:57]
	s_nop 0
	v_pk_mul_f32 v[54:55], v[66:67], v[54:55] op_sel_hi:[0,1]
	v_cvt_pk_f16_f32 v51, v54, v55
	s_waitcnt lgkmcnt(0)
	v_pk_fma_f32 v[54:55], v[58:59], v[62:63], v[152:153]
	s_nop 0
	v_pk_mul_f32 v[56:57], v[54:55], s[28:29] op_sel_hi:[1,0]
	v_pk_mul_f32 v[54:55], v[54:55], 0.5 op_sel_hi:[1,0]
	v_fma_f32 v52, |v56|, s74, 1.0
	v_fma_f32 v59, |v57|, s74, 1.0
	v_rcp_f32_e32 v58, v52
	v_rcp_f32_e32 v59, v59
	v_mul_f32_e64 v52, |v56|, -|v56|
	v_mul_f32_e32 v52, 0x3fb8aa3b, v52
	v_exp_f32_e32 v60, v52
	v_mul_f32_e64 v52, |v57|, -|v57|
	v_pk_fma_f32 v[62:63], v[58:59], s[40:41], v[158:159] op_sel_hi:[1,0,0]
	v_mul_f32_e32 v52, 0x3fb8aa3b, v52
	v_pk_fma_f32 v[62:63], v[58:59], v[62:63], s[42:43] op_sel_hi:[1,1,0]
	v_exp_f32_e32 v61, v52
	v_pk_fma_f32 v[62:63], v[58:59], v[62:63], s[44:45] op_sel_hi:[1,1,0]
	s_nop 0
	v_pk_fma_f32 v[62:63], v[58:59], v[62:63], s[46:47] op_sel_hi:[1,1,0]
	s_nop 0
	v_pk_mul_f32 v[58:59], v[62:63], v[58:59] neg_lo:[0,1] neg_hi:[0,1]
	s_nop 0
	v_pk_fma_f32 v[58:59], v[58:59], v[60:61], 1.0 op_sel_hi:[1,1,0]
	s_nop 0
	v_bfi_b32 v57, s71, v59, v57
	v_bfi_b32 v56, s71, v58, v56
	v_cvt_f32_f16_sdwa v59, v53 dst_sel:DWORD dst_unused:UNUSED_PAD src0_sel:WORD_1
	v_cvt_f32_f16_e32 v58, v53
	v_pk_add_f32 v[56:57], v[56:57], 1.0 op_sel_hi:[1,0]
	s_nop 0
	v_pk_mul_f32 v[52:53], v[54:55], v[56:57]
	v_pk_fma_f32 v[54:55], v[58:59], v[64:65], v[154:155]
	v_pk_mul_f32 v[52:53], v[66:67], v[52:53] op_sel_hi:[0,1]
	v_pk_mul_f32 v[56:57], v[54:55], s[28:29] op_sel_hi:[1,0]
	v_cvt_pk_f16_f32 v52, v52, v53
	v_fma_f32 v53, |v56|, s74, 1.0
	v_fma_f32 v59, |v57|, s74, 1.0
	v_rcp_f32_e32 v58, v53
	v_rcp_f32_e32 v59, v59
	v_mul_f32_e64 v53, |v56|, -|v56|
	v_mul_f32_e32 v53, 0x3fb8aa3b, v53
	v_exp_f32_e32 v60, v53
	v_mul_f32_e64 v53, |v57|, -|v57|
	v_pk_fma_f32 v[62:63], v[58:59], s[40:41], v[158:159] op_sel_hi:[1,0,0]
	v_mul_f32_e32 v53, 0x3fb8aa3b, v53
	v_pk_fma_f32 v[62:63], v[58:59], v[62:63], s[42:43] op_sel_hi:[1,1,0]
	v_exp_f32_e32 v61, v53
	v_pk_fma_f32 v[62:63], v[58:59], v[62:63], s[44:45] op_sel_hi:[1,1,0]
	v_pk_mul_f32 v[54:55], v[54:55], 0.5 op_sel_hi:[1,0]
	v_pk_fma_f32 v[62:63], v[58:59], v[62:63], s[46:47] op_sel_hi:[1,1,0]
	s_nop 0
	v_pk_mul_f32 v[58:59], v[62:63], v[58:59] neg_lo:[0,1] neg_hi:[0,1]
	s_nop 0
	v_pk_fma_f32 v[58:59], v[58:59], v[60:61], 1.0 op_sel_hi:[1,1,0]
	s_nop 0
	v_bfi_b32 v57, s71, v59, v57
	v_bfi_b32 v56, s71, v58, v56
	v_pk_add_f32 v[56:57], v[56:57], 1.0 op_sel_hi:[1,0]
	s_nop 0
	v_pk_mul_f32 v[54:55], v[54:55], v[56:57]
	s_nop 0
	v_pk_mul_f32 v[54:55], v[66:67], v[54:55] op_sel_hi:[0,1]
	v_cvt_pk_f16_f32 v53, v54, v55
	ds_write_b128 v141, v[50:53]
	s_or_b64 exec, exec, s[20:21]
	s_and_saveexec_b64 s[20:21], s[14:15]
	s_cbranch_execz .LBB3_10
.LBB3_37:
	s_waitcnt vmcnt(12)
	ds_read_b128 v[50:53], v121 offset:62400
	ds_read_b128 v[54:57], v121 offset:63104
	s_waitcnt vmcnt(11)
	v_cvt_f32_f16_sdwa v111, v46 dst_sel:DWORD dst_unused:UNUSED_PAD src0_sel:WORD_1
	v_cvt_f32_f16_e32 v110, v46
	v_mov_b64_e32 v[154:155], s[34:35]
	v_add_u32_e32 v58, s58, v115
	v_cmp_gt_u32_e32 vcc, s73, v58
	s_waitcnt lgkmcnt(0)
	v_pk_fma_f32 v[50:51], v[110:111], v[50:51], v[54:55]
	ds_read_b128 v[58:61], v121 offset:62416
	ds_read_b128 v[62:65], v121 offset:63120
	v_pk_mul_f32 v[54:55], v[50:51], s[28:29] op_sel_hi:[1,0]
	v_pk_mul_f32 v[50:51], v[50:51], 0.5 op_sel_hi:[1,0]
	v_fma_f32 v46, |v54|, s74, 1.0
	v_fma_f32 v107, |v55|, s74, 1.0
	v_rcp_f32_e32 v110, v46
	v_rcp_f32_e32 v111, v107
	v_mul_f32_e64 v46, |v54|, -|v54|
	v_mul_f32_e32 v46, 0x3fb8aa3b, v46
	v_exp_f32_e32 v152, v46
	v_mul_f32_e64 v46, |v55|, -|v55|
	v_pk_fma_f32 v[156:157], v[110:111], s[40:41], v[154:155] op_sel_hi:[1,0,0]
	v_mul_f32_e32 v46, 0x3fb8aa3b, v46
	v_pk_fma_f32 v[156:157], v[110:111], v[156:157], s[42:43] op_sel_hi:[1,1,0]
	v_exp_f32_e32 v153, v46
	v_pk_fma_f32 v[156:157], v[110:111], v[156:157], s[44:45] op_sel_hi:[1,1,0]
	v_cndmask_b32_e64 v66, 0, 1.0, vcc
	v_pk_fma_f32 v[156:157], v[110:111], v[156:157], s[46:47] op_sel_hi:[1,1,0]
	s_nop 0
	v_pk_mul_f32 v[110:111], v[156:157], v[110:111] neg_lo:[0,1] neg_hi:[0,1]
	s_nop 0
	v_pk_fma_f32 v[110:111], v[110:111], v[152:153], 1.0 op_sel_hi:[1,1,0]
	s_nop 0
	v_bfi_b32 v55, s71, v111, v55
	v_bfi_b32 v54, s71, v110, v54
	v_cvt_f32_f16_sdwa v111, v47 dst_sel:DWORD dst_unused:UNUSED_PAD src0_sel:WORD_1
	v_cvt_f32_f16_e32 v110, v47
	v_pk_add_f32 v[54:55], v[54:55], 1.0 op_sel_hi:[1,0]
	s_nop 0
	v_pk_mul_f32 v[46:47], v[50:51], v[54:55]
	v_pk_fma_f32 v[50:51], v[110:111], v[52:53], v[56:57]
	v_pk_mul_f32 v[46:47], v[66:67], v[46:47] op_sel_hi:[0,1]
	v_pk_mul_f32 v[52:53], v[50:51], s[28:29] op_sel_hi:[1,0]
	v_cvt_pk_f16_f32 v46, v46, v47
	v_fma_f32 v47, |v52|, s74, 1.0
	v_fma_f32 v55, |v53|, s74, 1.0
	v_rcp_f32_e32 v54, v47
	v_rcp_f32_e32 v55, v55
	v_mul_f32_e64 v47, |v52|, -|v52|
	v_mul_f32_e32 v47, 0x3fb8aa3b, v47
	v_exp_f32_e32 v56, v47
	v_mul_f32_e64 v47, |v53|, -|v53|
	v_pk_fma_f32 v[110:111], v[54:55], s[40:41], v[154:155] op_sel_hi:[1,0,0]
	v_mul_f32_e32 v47, 0x3fb8aa3b, v47
	v_pk_fma_f32 v[110:111], v[54:55], v[110:111], s[42:43] op_sel_hi:[1,1,0]
	v_exp_f32_e32 v57, v47
	v_pk_fma_f32 v[110:111], v[54:55], v[110:111], s[44:45] op_sel_hi:[1,1,0]
	v_pk_mul_f32 v[50:51], v[50:51], 0.5 op_sel_hi:[1,0]
	v_pk_fma_f32 v[110:111], v[54:55], v[110:111], s[46:47] op_sel_hi:[1,1,0]
	s_nop 0
	v_pk_mul_f32 v[54:55], v[110:111], v[54:55] neg_lo:[0,1] neg_hi:[0,1]
	s_nop 0
	v_pk_fma_f32 v[54:55], v[54:55], v[56:57], 1.0 op_sel_hi:[1,1,0]
	s_nop 0
	v_bfi_b32 v53, s71, v55, v53
	v_bfi_b32 v52, s71, v54, v52
	v_cvt_f32_f16_sdwa v55, v48 dst_sel:DWORD dst_unused:UNUSED_PAD src0_sel:WORD_1
	v_cvt_f32_f16_e32 v54, v48
	v_pk_add_f32 v[52:53], v[52:53], 1.0 op_sel_hi:[1,0]
	s_nop 0
	v_pk_mul_f32 v[50:51], v[50:51], v[52:53]
	s_nop 0
	v_pk_mul_f32 v[50:51], v[66:67], v[50:51] op_sel_hi:[0,1]
	v_cvt_pk_f16_f32 v47, v50, v51
	s_waitcnt lgkmcnt(0)
	v_pk_fma_f32 v[50:51], v[54:55], v[58:59], v[62:63]
	s_nop 0
	v_pk_mul_f32 v[52:53], v[50:51], s[28:29] op_sel_hi:[1,0]
	v_pk_mul_f32 v[50:51], v[50:51], 0.5 op_sel_hi:[1,0]
	v_fma_f32 v48, |v52|, s74, 1.0
	v_fma_f32 v55, |v53|, s74, 1.0
	v_rcp_f32_e32 v54, v48
	v_rcp_f32_e32 v55, v55
	v_mul_f32_e64 v48, |v52|, -|v52|
	v_mul_f32_e32 v48, 0x3fb8aa3b, v48
	v_exp_f32_e32 v56, v48
	v_mul_f32_e64 v48, |v53|, -|v53|
	v_pk_fma_f32 v[58:59], v[54:55], s[40:41], v[154:155] op_sel_hi:[1,0,0]
	v_mul_f32_e32 v48, 0x3fb8aa3b, v48
	v_pk_fma_f32 v[58:59], v[54:55], v[58:59], s[42:43] op_sel_hi:[1,1,0]
	v_exp_f32_e32 v57, v48
	v_pk_fma_f32 v[58:59], v[54:55], v[58:59], s[44:45] op_sel_hi:[1,1,0]
	s_nop 0
	v_pk_fma_f32 v[58:59], v[54:55], v[58:59], s[46:47] op_sel_hi:[1,1,0]
	s_nop 0
	v_pk_mul_f32 v[54:55], v[58:59], v[54:55] neg_lo:[0,1] neg_hi:[0,1]
	s_nop 0
	v_pk_fma_f32 v[54:55], v[54:55], v[56:57], 1.0 op_sel_hi:[1,1,0]
	s_nop 0
	v_bfi_b32 v53, s71, v55, v53
	v_bfi_b32 v52, s71, v54, v52
	v_cvt_f32_f16_sdwa v55, v49 dst_sel:DWORD dst_unused:UNUSED_PAD src0_sel:WORD_1
	v_cvt_f32_f16_e32 v54, v49
	v_pk_add_f32 v[52:53], v[52:53], 1.0 op_sel_hi:[1,0]
	s_nop 0
	v_pk_mul_f32 v[48:49], v[50:51], v[52:53]
	v_pk_fma_f32 v[50:51], v[54:55], v[60:61], v[64:65]
	v_pk_mul_f32 v[48:49], v[66:67], v[48:49] op_sel_hi:[0,1]
	v_pk_mul_f32 v[52:53], v[50:51], s[28:29] op_sel_hi:[1,0]
	v_cvt_pk_f16_f32 v48, v48, v49
	v_fma_f32 v49, |v52|, s74, 1.0
	v_fma_f32 v55, |v53|, s74, 1.0
	v_rcp_f32_e32 v54, v49
	v_rcp_f32_e32 v55, v55
	v_mul_f32_e64 v49, |v52|, -|v52|
	v_mul_f32_e32 v49, 0x3fb8aa3b, v49
	v_exp_f32_e32 v56, v49
	v_mul_f32_e64 v49, |v53|, -|v53|
	v_pk_fma_f32 v[58:59], v[54:55], s[40:41], v[154:155] op_sel_hi:[1,0,0]
	v_mul_f32_e32 v49, 0x3fb8aa3b, v49
	v_pk_fma_f32 v[58:59], v[54:55], v[58:59], s[42:43] op_sel_hi:[1,1,0]
	v_exp_f32_e32 v57, v49
	v_pk_fma_f32 v[58:59], v[54:55], v[58:59], s[44:45] op_sel_hi:[1,1,0]
	v_pk_mul_f32 v[50:51], v[50:51], 0.5 op_sel_hi:[1,0]
	v_pk_fma_f32 v[58:59], v[54:55], v[58:59], s[46:47] op_sel_hi:[1,1,0]
	s_nop 0
	v_pk_mul_f32 v[54:55], v[58:59], v[54:55] neg_lo:[0,1] neg_hi:[0,1]
	s_nop 0
	v_pk_fma_f32 v[54:55], v[54:55], v[56:57], 1.0 op_sel_hi:[1,1,0]
	s_nop 0
	v_bfi_b32 v53, s71, v55, v53
	v_bfi_b32 v52, s71, v54, v52
	v_pk_add_f32 v[52:53], v[52:53], 1.0 op_sel_hi:[1,0]
	s_nop 0
	v_pk_mul_f32 v[50:51], v[50:51], v[52:53]
	s_nop 0
	v_pk_mul_f32 v[50:51], v[66:67], v[50:51] op_sel_hi:[0,1]
	v_cvt_pk_f16_f32 v49, v50, v51
	ds_write_b128 v142, v[46:49]
	s_or_b64 exec, exec, s[20:21]
	s_and_saveexec_b64 s[20:21], s[16:17]
	s_cbranch_execnz .LBB3_11
	s_branch .LBB3_12
